# hmpost (P4) token loop unrolled, loads two tokens ahead
# baseline (speedup 1.0000x reference)
.LBB0_615:
	s_cmp_lt_i32 s48, 5
	s_cselect_b64 s[6:7], -1, 0
	s_and_b64 s[10:11], s[6:7], s[4:5]
	s_andn2_b64 vcc, exec, s[10:11]
	s_cbranch_vccnz .LBB0_620
	v_lshrrev_b32_e32 v1, 6, v0
	s_waitcnt vmcnt(3)
	v_lshl_or_b32 v18, s2, 3, v1
	s_movk_i32 s4, 0x4000
	v_cmp_gt_i32_e32 vcc, s4, v18
	s_and_saveexec_b64 s[12:13], vcc
	s_cbranch_execz .LBB0_619
	s_load_dwordx2 s[4:5], s[0:1], 0x30
	v_lshlrev_b32_e32 v1, 4, v0
	v_and_b32_e32 v1, 0x3f0, v1
	s_lshl_b32 s14, s3, 3
	s_movk_i32 s6, 0x4c00
	s_waitcnt lgkmcnt(0)
	global_load_dwordx4 v[2:5], v1, s[4:5] offset:3072
	global_load_dwordx4 v[6:9], v1, s[4:5] offset:2048
	global_load_dwordx4 v[10:13], v1, s[4:5] offset:1024
	global_load_dwordx4 v[14:17], v1, s[4:5]
	v_mbcnt_lo_u32_b32 v1, -1, 0
	v_mbcnt_hi_u32_b32 v19, -1, v1
	v_and_b32_e32 v1, 64, v19
	v_add_u32_e32 v20, 64, v1
	v_xor_b32_e32 v1, 32, v19
	v_cmp_lt_i32_e32 vcc, v1, v20
	v_xor_b32_e32 v21, 16, v19
	s_load_dwordx2 s[4:5], s[0:1], 0xb0
	v_cndmask_b32_e32 v1, v19, v1, vcc
	v_cmp_lt_i32_e32 vcc, v21, v20
	s_ashr_i32 s15, s14, 31
	v_lshlrev_b32_e32 v1, 2, v1
	v_cndmask_b32_e32 v21, v19, v21, vcc
	v_lshlrev_b32_e32 v34, 2, v21
	v_xor_b32_e32 v21, 8, v19
	v_cmp_lt_i32_e32 vcc, v21, v20
	s_waitcnt vmcnt(6) lgkmcnt(0)
	v_mov_b64_e32 v[22:23], s[4:5]
	v_mad_i64_i32 v[22:23], s[6:7], v18, s6, v[22:23]
	v_cndmask_b32_e32 v21, v19, v21, vcc
	v_lshlrev_b32_e32 v35, 2, v21
	v_xor_b32_e32 v21, 4, v19
	v_cmp_lt_i32_e32 vcc, v21, v20
	s_mul_i32 s16, s3, 0x26000
	s_mul_hi_i32 s17, s14, 0x4c00
	v_cndmask_b32_e32 v21, v19, v21, vcc
	v_lshlrev_b32_e32 v36, 2, v21
	v_xor_b32_e32 v21, 2, v19
	v_cmp_lt_i32_e32 vcc, v21, v20
	s_lshl_b64 s[18:19], s[14:15], 11
	s_mov_b64 s[20:21], 0
	v_cndmask_b32_e32 v21, v19, v21, vcc
	v_lshlrev_b32_e32 v37, 2, v21
	v_xor_b32_e32 v21, 1, v19
	v_cmp_lt_i32_e32 vcc, v21, v20
	s_mov_b32 s22, 0x3b800000
	s_mov_b32 s15, 0x800000
	v_cndmask_b32_e32 v19, v19, v21, vcc
	v_lshlrev_b32_e32 v38, 2, v19
	v_and_b32_e32 v19, 63, v0
	v_lshlrev_b32_e32 v20, 3, v19
	v_ashrrev_i32_e32 v19, 31, v18
	v_lshlrev_b64 v[24:25], 11, v[18:19]
	v_lshl_add_u64 v[24:25], s[4:5], 0, v[24:25]
	s_mov_b32 s4, 0x358637bd
	v_mov_b32_e32 v21, 0
	s_mov_b32 s23, 0x2b80a000
	s_movk_i32 s24, 0x3fff
	s_waitcnt vmcnt(5)
	v_mov_b64_e32 v[26:27], s[4:5]
	v_lshl_add_u64 v[228:229], v[24:25], 0, v[20:21]
	v_lshl_add_u64 v[230:231], v[22:23], 0, v[20:21]
	v_add_co_u32_e32 v228, vcc, 0x3ec4a000, v228
	s_nop 1
	v_addc_co_u32_e32 v229, vcc, 0, v229, vcc
	v_add_co_u32_e32 v230, vcc, 0x42c4b000, v230
	s_nop 1
	v_addc_co_u32_e32 v231, vcc, 0, v231, vcc
	global_load_dwordx2 v[96:97], v[228:229], off
	global_load_dwordx2 v[98:99], v[228:229], off offset:512
	global_load_dwordx2 v[100:101], v[228:229], off offset:1024
	global_load_dwordx2 v[102:103], v[228:229], off offset:1536
	global_load_dwordx2 v[104:105], v[230:231], off offset:2048
	global_load_dwordx2 v[106:107], v[230:231], off offset:2560
	global_load_dwordx2 v[108:109], v[230:231], off offset:3072
	global_load_dwordx2 v[110:111], v[230:231], off offset:3584
	v_lshl_add_u64 v[228:229], v[228:229], 0, s[18:19]
	v_lshl_add_u64 v[230:231], v[230:231], 0, s[16:17]
	global_load_dwordx2 v[112:113], v[228:229], off
	global_load_dwordx2 v[114:115], v[228:229], off offset:512
	global_load_dwordx2 v[116:117], v[228:229], off offset:1024
	global_load_dwordx2 v[118:119], v[228:229], off offset:1536
	global_load_dwordx2 v[120:121], v[230:231], off offset:2048
	global_load_dwordx2 v[122:123], v[230:231], off offset:2560
	global_load_dwordx2 v[124:125], v[230:231], off offset:3072
	global_load_dwordx2 v[126:127], v[230:231], off offset:3584
	v_lshl_add_u64 v[228:229], v[228:229], 0, s[18:19]
	v_lshl_add_u64 v[230:231], v[230:231], 0, s[16:17]
	s_nop 0
	v_lshl_add_u64 v[30:31], v[24:25], 0, v[20:21]
	v_add_co_u32_e32 v40, vcc, 0x3ec4a000, v30
	v_lshl_add_u64 v[28:29], v[22:23], 0, v[20:21]
	v_add_co_u32_e64 v32, s[4:5], s23, v30
	v_addc_co_u32_e32 v41, vcc, 0, v31, vcc
	s_nop 0
	v_addc_co_u32_e64 v33, s[4:5], 0, v31, s[4:5]
	v_add_co_u32_e32 v28, vcc, 0x42c4b000, v28
	s_waitcnt vmcnt(8)
	v_mov_b32_e32 v30, v96
	v_mov_b32_e32 v31, v97
	v_mov_b32_e32 v42, v98
	v_mov_b32_e32 v43, v99
	v_mov_b32_e32 v44, v100
	v_mov_b32_e32 v45, v101
	v_mov_b32_e32 v46, v102
	v_mov_b32_e32 v47, v103
	v_mov_b32_e32 v40, v104
	v_mov_b32_e32 v41, v105
	v_mov_b32_e32 v48, v106
	v_mov_b32_e32 v49, v107
	v_mov_b32_e32 v50, v108
	v_mov_b32_e32 v51, v109
	v_mov_b32_e32 v52, v110
	v_mov_b32_e32 v53, v111
	global_load_dwordx2 v[128:129], v[228:229], off
	global_load_dwordx2 v[130:131], v[228:229], off offset:512
	global_load_dwordx2 v[132:133], v[228:229], off offset:1024
	global_load_dwordx2 v[134:135], v[228:229], off offset:1536
	global_load_dwordx2 v[136:137], v[230:231], off offset:2048
	global_load_dwordx2 v[138:139], v[230:231], off offset:2560
	global_load_dwordx2 v[140:141], v[230:231], off offset:3072
	global_load_dwordx2 v[142:143], v[230:231], off offset:3584
	v_lshl_add_u64 v[228:229], v[228:229], 0, s[18:19]
	v_lshl_add_u64 v[230:231], v[230:231], 0, s[16:17]
	v_addc_co_u32_e32 v29, vcc, 0, v29, vcc
	v_add_u32_e32 v18, s14, v18
	v_cmp_lt_i32_e64 s[4:5], s24, v18
	s_or_b64 s[20:21], s[4:5], s[20:21]
	v_lshl_add_u64 v[22:23], v[22:23], 0, s[16:17]
	v_lshl_add_u64 v[24:25], v[24:25], 0, s[18:19]
	s_nop 0
	v_lshlrev_b32_e32 v28, 16, v30
	v_and_b32_e32 v29, 0xffff0000, v30
	s_nop 0
	v_lshlrev_b32_e32 v54, 16, v42
	v_and_b32_e32 v55, 0xffff0000, v42
	v_and_b32_e32 v30, 0xffff0000, v31
	v_lshlrev_b32_e32 v31, 16, v31
	v_and_b32_e32 v42, 0xffff0000, v43
	v_lshlrev_b32_e32 v43, 16, v43
	v_pk_mul_f32 v[60:61], v[28:29], v[28:29]
	v_pk_mul_f32 v[64:65], v[54:55], v[54:55]
	s_nop 0
	v_lshlrev_b32_e32 v19, 16, v40
	v_and_b32_e32 v39, 0xffff0000, v40
	v_lshlrev_b32_e32 v40, 16, v41
	v_and_b32_e32 v41, 0xffff0000, v41
	v_lshlrev_b32_e32 v56, 16, v44
	v_and_b32_e32 v57, 0xffff0000, v44
	v_lshlrev_b32_e32 v58, 16, v46
	v_and_b32_e32 v59, 0xffff0000, v46
	v_pk_mul_f32 v[62:63], v[30:31], v[30:31]
	v_pk_mul_f32 v[66:67], v[42:43], v[42:43]
	v_mul_f32_e32 v86, 0xbfb8aa3b, v40
	v_mul_f32_e32 v87, 0xbfb8aa3b, v41
	v_mov_b32_e32 v40, v64
	v_mov_b32_e32 v41, v60
	v_mov_b32_e32 v60, v65
	v_and_b32_e32 v44, 0xffff0000, v45
	v_lshlrev_b32_e32 v45, 16, v45
	v_and_b32_e32 v46, 0xffff0000, v47
	v_lshlrev_b32_e32 v47, 16, v47
	v_pk_mul_f32 v[68:69], v[56:57], v[56:57]
	v_pk_mul_f32 v[72:73], v[58:59], v[58:59]
	s_nop 0
	v_lshlrev_b32_e32 v76, 16, v48
	v_and_b32_e32 v77, 0xffff0000, v48
	v_lshlrev_b32_e32 v78, 16, v49
	v_and_b32_e32 v79, 0xffff0000, v49
	s_nop 0
	v_lshlrev_b32_e32 v80, 16, v50
	v_and_b32_e32 v50, 0xffff0000, v50
	v_lshlrev_b32_e32 v81, 16, v51
	v_and_b32_e32 v51, 0xffff0000, v51
	v_mov_b32_e32 v48, v67
	v_mov_b32_e32 v49, v63
	v_pk_add_f32 v[40:41], v[40:41], v[60:61]
	v_pk_mul_f32 v[70:71], v[44:45], v[44:45]
	v_pk_mul_f32 v[74:75], v[46:47], v[46:47]
	v_mov_b32_e32 v67, v62
	v_mul_f32_e32 v63, 0xbfb8aa3b, v77
	v_mul_f32_e32 v65, 0xbfb8aa3b, v79
	v_mul_f32_e32 v77, 0xbfb8aa3b, v50
	v_mul_f32_e32 v79, 0xbfb8aa3b, v51
	v_mov_b32_e32 v50, v72
	v_mov_b32_e32 v51, v68
	v_mov_b32_e32 v68, v73
	v_pk_add_f32 v[40:41], v[48:49], v[40:41]
	s_nop 0
	v_lshlrev_b32_e32 v82, 16, v52
	v_and_b32_e32 v83, 0xffff0000, v52
	v_lshlrev_b32_e32 v84, 16, v53
	v_and_b32_e32 v85, 0xffff0000, v53
	v_mov_b32_e32 v52, v75
	v_mov_b32_e32 v53, v71
	v_pk_add_f32 v[50:51], v[50:51], v[68:69]
	v_pk_add_f32 v[40:41], v[66:67], v[40:41]
	v_pk_add_f32 v[48:49], v[52:53], v[50:51]
	ds_bpermute_b32 v51, v1, v41
	ds_bpermute_b32 v50, v1, v40
	v_mov_b32_e32 v75, v70
	v_pk_add_f32 v[48:49], v[74:75], v[48:49]
	ds_bpermute_b32 v53, v1, v49
	ds_bpermute_b32 v52, v1, v48
	s_waitcnt lgkmcnt(2)
	v_pk_add_f32 v[40:41], v[40:41], v[50:51]
	ds_bpermute_b32 v51, v34, v41
	ds_bpermute_b32 v50, v34, v40
	v_mul_f32_e32 v19, 0xbfb8aa3b, v19
	s_waitcnt lgkmcnt(2)
	v_pk_add_f32 v[48:49], v[48:49], v[52:53]
	ds_bpermute_b32 v53, v34, v49
	ds_bpermute_b32 v52, v34, v48
	s_waitcnt lgkmcnt(2)
	v_pk_add_f32 v[40:41], v[40:41], v[50:51]
	ds_bpermute_b32 v51, v35, v41
	ds_bpermute_b32 v50, v35, v40
	v_mul_f32_e32 v39, 0xbfb8aa3b, v39
	s_waitcnt lgkmcnt(2)
	v_pk_add_f32 v[48:49], v[48:49], v[52:53]
	ds_bpermute_b32 v53, v35, v49
	ds_bpermute_b32 v52, v35, v48
	s_waitcnt lgkmcnt(2)
	v_pk_add_f32 v[40:41], v[40:41], v[50:51]
	ds_bpermute_b32 v51, v36, v41
	ds_bpermute_b32 v50, v36, v40
	v_mul_f32_e32 v62, 0xbfb8aa3b, v76
	s_waitcnt lgkmcnt(2)
	v_pk_add_f32 v[48:49], v[48:49], v[52:53]
	ds_bpermute_b32 v53, v36, v49
	ds_bpermute_b32 v52, v36, v48
	s_waitcnt lgkmcnt(2)
	v_pk_add_f32 v[40:41], v[40:41], v[50:51]
	ds_bpermute_b32 v51, v37, v41
	ds_bpermute_b32 v50, v37, v40
	v_mul_f32_e32 v76, 0xbfb8aa3b, v80
	s_waitcnt lgkmcnt(2)
	v_pk_add_f32 v[48:49], v[48:49], v[52:53]
	ds_bpermute_b32 v53, v37, v49
	ds_bpermute_b32 v52, v37, v48
	s_waitcnt lgkmcnt(2)
	v_pk_add_f32 v[40:41], v[40:41], v[50:51]
	ds_bpermute_b32 v51, v38, v41
	ds_bpermute_b32 v50, v38, v40
	v_exp_f32_e32 v19, v19
	s_waitcnt lgkmcnt(2)
	v_pk_add_f32 v[48:49], v[48:49], v[52:53]
	ds_bpermute_b32 v53, v38, v49
	ds_bpermute_b32 v52, v38, v48
	s_waitcnt lgkmcnt(2)
	v_pk_add_f32 v[40:41], v[40:41], v[50:51]
	v_exp_f32_e32 v39, v39
	v_pk_fma_f32 v[40:41], v[40:41], s[22:23], v[26:27] op_sel_hi:[1,0,0]
	v_exp_f32_e32 v80, v86
	v_mul_f32_e32 v50, 0x4b800000, v41
	v_cmp_gt_f32_e64 s[8:9], s15, v41
	s_waitcnt lgkmcnt(0)
	v_pk_add_f32 v[48:49], v[48:49], v[52:53]
	v_mul_f32_e32 v64, 0xbfb8aa3b, v78
	v_cndmask_b32_e64 v41, v41, v50, s[8:9]
	v_mul_f32_e32 v78, 0xbfb8aa3b, v81
	v_exp_f32_e32 v81, v87
	v_pk_fma_f32 v[48:49], v[48:49], s[22:23], v[26:27] op_sel_hi:[1,0,0]
	v_mul_f32_e32 v51, 0x4b800000, v40
	v_cmp_gt_f32_e32 vcc, s15, v40
	v_rsq_f32_e32 v41, v41
	v_exp_f32_e32 v60, v62
	v_exp_f32_e32 v61, v63
	v_exp_f32_e32 v62, v64
	v_exp_f32_e32 v63, v65
	v_mul_f32_e32 v52, 0x4b800000, v49
	v_mul_f32_e32 v53, 0x4b800000, v48
	v_cmp_gt_f32_e64 s[4:5], s15, v48
	v_cmp_gt_f32_e64 s[6:7], s15, v49
	v_cndmask_b32_e32 v40, v40, v51, vcc
	v_mul_f32_e32 v70, 0xbfb8aa3b, v82
	v_mul_f32_e32 v71, 0xbfb8aa3b, v83
	v_mul_f32_e32 v72, 0xbfb8aa3b, v84
	v_mul_f32_e32 v73, 0xbfb8aa3b, v85
	v_exp_f32_e32 v64, v76
	v_exp_f32_e32 v65, v77
	v_exp_f32_e32 v76, v78
	v_exp_f32_e32 v77, v79
	v_cndmask_b32_e64 v49, v49, v52, s[6:7]
	v_cndmask_b32_e64 v48, v48, v53, s[4:5]
	v_rsq_f32_e32 v40, v40
	v_exp_f32_e32 v68, v70
	v_exp_f32_e32 v69, v71
	v_exp_f32_e32 v70, v72
	v_exp_f32_e32 v71, v73
	v_add_f32_e32 v19, 1.0, v19
	v_add_f32_e32 v39, 1.0, v39
	v_add_f32_e32 v66, 1.0, v80
	v_rsq_f32_e32 v49, v49
	v_rsq_f32_e32 v48, v48
	v_add_f32_e32 v67, 1.0, v81
	v_rcp_f32_e32 v19, v19
	v_rcp_f32_e32 v39, v39
	v_rcp_f32_e32 v66, v66
	v_mul_f32_e32 v50, 0x45800000, v41
	v_add_f32_e32 v60, 1.0, v60
	v_add_f32_e32 v61, 1.0, v61
	v_add_f32_e32 v62, 1.0, v62
	v_add_f32_e32 v63, 1.0, v63
	v_rcp_f32_e32 v67, v67
	v_cndmask_b32_e64 v41, v41, v50, s[8:9]
	v_add_f32_e32 v64, 1.0, v64
	v_add_f32_e32 v65, 1.0, v65
	v_add_f32_e32 v72, 1.0, v76
	v_add_f32_e32 v73, 1.0, v77
	v_rcp_f32_e32 v60, v60
	v_rcp_f32_e32 v61, v61
	v_rcp_f32_e32 v62, v62
	v_rcp_f32_e32 v63, v63
	v_mul_f32_e32 v51, 0x45800000, v40
	v_mul_f32_e32 v28, v41, v28
	v_mul_f32_e32 v29, v41, v29
	v_mul_f32_e32 v31, v41, v31
	v_add_f32_e32 v68, 1.0, v68
	v_add_f32_e32 v69, 1.0, v69
	v_add_f32_e32 v70, 1.0, v70
	v_add_f32_e32 v71, 1.0, v71
	v_rcp_f32_e32 v64, v64
	v_rcp_f32_e32 v65, v65
	v_rcp_f32_e32 v72, v72
	v_rcp_f32_e32 v73, v73
	v_mul_f32_e32 v52, 0x45800000, v49
	v_mul_f32_e32 v53, 0x45800000, v48
	v_cndmask_b32_e32 v40, v40, v51, vcc
	v_mul_f32_e32 v30, v41, v30
	v_mul_f32_e32 v28, v14, v28
	v_mul_f32_e32 v29, v15, v29
	v_mul_f32_e32 v31, v16, v31
	v_rcp_f32_e32 v68, v68
	v_rcp_f32_e32 v69, v69
	v_rcp_f32_e32 v70, v70
	v_rcp_f32_e32 v71, v71
	v_cndmask_b32_e64 v49, v49, v52, s[6:7]
	v_cndmask_b32_e64 v48, v48, v53, s[4:5]
	v_mul_f32_e32 v41, v40, v54
	v_mul_f32_e32 v50, v40, v55
	v_mul_f32_e32 v43, v40, v43
	v_mul_f32_e32 v40, v40, v42
	v_mul_f32_e32 v30, v17, v30
	v_mul_f32_e32 v19, v19, v28
	v_mul_f32_e32 v28, v39, v29
	v_mul_f32_e32 v29, v66, v31
	v_mul_f32_e32 v42, v49, v56
	v_mul_f32_e32 v51, v49, v57
	v_mul_f32_e32 v45, v49, v45
	v_mul_f32_e32 v44, v49, v44
	v_mul_f32_e32 v49, v48, v58
	v_mul_f32_e32 v52, v48, v59
	v_mul_f32_e32 v47, v48, v47
	v_mul_f32_e32 v46, v48, v46
	v_mul_f32_e32 v41, v10, v41
	v_mul_f32_e32 v48, v11, v50
	v_mul_f32_e32 v43, v12, v43
	v_mul_f32_e32 v40, v13, v40
	v_mul_f32_e32 v30, v67, v30
	v_cvt_pk_bf16_f32 v28, v19, v28
	v_cvt_pk_bf16_f32 v29, v29, v30
	v_mul_f32_e32 v42, v6, v42
	v_mul_f32_e32 v50, v7, v51
	v_mul_f32_e32 v45, v8, v45
	v_mul_f32_e32 v44, v9, v44
	v_mul_f32_e32 v31, v60, v41
	v_mul_f32_e32 v39, v61, v48
	v_mul_f32_e32 v41, v62, v43
	v_mul_f32_e32 v40, v63, v40
	global_store_dwordx2 v[32:33], v[28:29], off
	v_cvt_pk_bf16_f32 v28, v31, v39
	v_cvt_pk_bf16_f32 v29, v41, v40
	v_mul_f32_e32 v49, v2, v49
	v_mul_f32_e32 v51, v3, v52
	v_mul_f32_e32 v47, v4, v47
	v_mul_f32_e32 v46, v5, v46
	v_mul_f32_e32 v42, v64, v42
	v_mul_f32_e32 v43, v65, v50
	v_mul_f32_e32 v45, v72, v45
	v_mul_f32_e32 v44, v73, v44
	global_store_dwordx2 v[32:33], v[28:29], off offset:512
	v_cvt_pk_bf16_f32 v28, v42, v43
	v_cvt_pk_bf16_f32 v29, v45, v44
	v_mul_f32_e32 v48, v68, v49
	v_mul_f32_e32 v49, v69, v51
	v_mul_f32_e32 v47, v70, v47
	v_mul_f32_e32 v46, v71, v46
	global_store_dwordx2 v[32:33], v[28:29], off offset:1024
	v_cvt_pk_bf16_f32 v28, v48, v49
	v_cvt_pk_bf16_f32 v29, v47, v46
	global_store_dwordx2 v[32:33], v[28:29], off offset:1536
	s_andn2_b64 exec, exec, s[20:21]
	s_nop 0
	v_lshl_add_u64 v[30:31], v[24:25], 0, v[20:21]
	v_add_co_u32_e32 v40, vcc, 0x3ec4a000, v30
	v_lshl_add_u64 v[28:29], v[22:23], 0, v[20:21]
	v_add_co_u32_e64 v32, s[4:5], s23, v30
	v_addc_co_u32_e32 v41, vcc, 0, v31, vcc
	s_nop 0
	v_addc_co_u32_e64 v33, s[4:5], 0, v31, s[4:5]
	v_add_co_u32_e32 v28, vcc, 0x42c4b000, v28
	s_waitcnt vmcnt(12)
	v_mov_b32_e32 v30, v112
	v_mov_b32_e32 v31, v113
	v_mov_b32_e32 v42, v114
	v_mov_b32_e32 v43, v115
	v_mov_b32_e32 v44, v116
	v_mov_b32_e32 v45, v117
	v_mov_b32_e32 v46, v118
	v_mov_b32_e32 v47, v119
	v_mov_b32_e32 v40, v120
	v_mov_b32_e32 v41, v121
	v_mov_b32_e32 v48, v122
	v_mov_b32_e32 v49, v123
	v_mov_b32_e32 v50, v124
	v_mov_b32_e32 v51, v125
	v_mov_b32_e32 v52, v126
	v_mov_b32_e32 v53, v127
	global_load_dwordx2 v[144:145], v[228:229], off
	global_load_dwordx2 v[146:147], v[228:229], off offset:512
	global_load_dwordx2 v[148:149], v[228:229], off offset:1024
	global_load_dwordx2 v[150:151], v[228:229], off offset:1536
	global_load_dwordx2 v[152:153], v[230:231], off offset:2048
	global_load_dwordx2 v[154:155], v[230:231], off offset:2560
	global_load_dwordx2 v[156:157], v[230:231], off offset:3072
	global_load_dwordx2 v[158:159], v[230:231], off offset:3584
	v_lshl_add_u64 v[228:229], v[228:229], 0, s[18:19]
	v_lshl_add_u64 v[230:231], v[230:231], 0, s[16:17]
	v_addc_co_u32_e32 v29, vcc, 0, v29, vcc
	v_add_u32_e32 v18, s14, v18
	v_cmp_lt_i32_e64 s[4:5], s24, v18
	s_or_b64 s[20:21], s[4:5], s[20:21]
	v_lshl_add_u64 v[22:23], v[22:23], 0, s[16:17]
	v_lshl_add_u64 v[24:25], v[24:25], 0, s[18:19]
	s_nop 0
	v_lshlrev_b32_e32 v28, 16, v30
	v_and_b32_e32 v29, 0xffff0000, v30
	s_nop 0
	v_lshlrev_b32_e32 v54, 16, v42
	v_and_b32_e32 v55, 0xffff0000, v42
	v_and_b32_e32 v30, 0xffff0000, v31
	v_lshlrev_b32_e32 v31, 16, v31
	v_and_b32_e32 v42, 0xffff0000, v43
	v_lshlrev_b32_e32 v43, 16, v43
	v_pk_mul_f32 v[60:61], v[28:29], v[28:29]
	v_pk_mul_f32 v[64:65], v[54:55], v[54:55]
	s_nop 0
	v_lshlrev_b32_e32 v19, 16, v40
	v_and_b32_e32 v39, 0xffff0000, v40
	v_lshlrev_b32_e32 v40, 16, v41
	v_and_b32_e32 v41, 0xffff0000, v41
	v_lshlrev_b32_e32 v56, 16, v44
	v_and_b32_e32 v57, 0xffff0000, v44
	v_lshlrev_b32_e32 v58, 16, v46
	v_and_b32_e32 v59, 0xffff0000, v46
	v_pk_mul_f32 v[62:63], v[30:31], v[30:31]
	v_pk_mul_f32 v[66:67], v[42:43], v[42:43]
	v_mul_f32_e32 v86, 0xbfb8aa3b, v40
	v_mul_f32_e32 v87, 0xbfb8aa3b, v41
	v_mov_b32_e32 v40, v64
	v_mov_b32_e32 v41, v60
	v_mov_b32_e32 v60, v65
	v_and_b32_e32 v44, 0xffff0000, v45
	v_lshlrev_b32_e32 v45, 16, v45
	v_and_b32_e32 v46, 0xffff0000, v47
	v_lshlrev_b32_e32 v47, 16, v47
	v_pk_mul_f32 v[68:69], v[56:57], v[56:57]
	v_pk_mul_f32 v[72:73], v[58:59], v[58:59]
	s_nop 0
	v_lshlrev_b32_e32 v76, 16, v48
	v_and_b32_e32 v77, 0xffff0000, v48
	v_lshlrev_b32_e32 v78, 16, v49
	v_and_b32_e32 v79, 0xffff0000, v49
	s_nop 0
	v_lshlrev_b32_e32 v80, 16, v50
	v_and_b32_e32 v50, 0xffff0000, v50
	v_lshlrev_b32_e32 v81, 16, v51
	v_and_b32_e32 v51, 0xffff0000, v51
	v_mov_b32_e32 v48, v67
	v_mov_b32_e32 v49, v63
	v_pk_add_f32 v[40:41], v[40:41], v[60:61]
	v_pk_mul_f32 v[70:71], v[44:45], v[44:45]
	v_pk_mul_f32 v[74:75], v[46:47], v[46:47]
	v_mov_b32_e32 v67, v62
	v_mul_f32_e32 v63, 0xbfb8aa3b, v77
	v_mul_f32_e32 v65, 0xbfb8aa3b, v79
	v_mul_f32_e32 v77, 0xbfb8aa3b, v50
	v_mul_f32_e32 v79, 0xbfb8aa3b, v51
	v_mov_b32_e32 v50, v72
	v_mov_b32_e32 v51, v68
	v_mov_b32_e32 v68, v73
	v_pk_add_f32 v[40:41], v[48:49], v[40:41]
	s_nop 0
	v_lshlrev_b32_e32 v82, 16, v52
	v_and_b32_e32 v83, 0xffff0000, v52
	v_lshlrev_b32_e32 v84, 16, v53
	v_and_b32_e32 v85, 0xffff0000, v53
	v_mov_b32_e32 v52, v75
	v_mov_b32_e32 v53, v71
	v_pk_add_f32 v[50:51], v[50:51], v[68:69]
	v_pk_add_f32 v[40:41], v[66:67], v[40:41]
	v_pk_add_f32 v[48:49], v[52:53], v[50:51]
	ds_bpermute_b32 v51, v1, v41
	ds_bpermute_b32 v50, v1, v40
	v_mov_b32_e32 v75, v70
	v_pk_add_f32 v[48:49], v[74:75], v[48:49]
	ds_bpermute_b32 v53, v1, v49
	ds_bpermute_b32 v52, v1, v48
	s_waitcnt lgkmcnt(2)
	v_pk_add_f32 v[40:41], v[40:41], v[50:51]
	ds_bpermute_b32 v51, v34, v41
	ds_bpermute_b32 v50, v34, v40
	v_mul_f32_e32 v19, 0xbfb8aa3b, v19
	s_waitcnt lgkmcnt(2)
	v_pk_add_f32 v[48:49], v[48:49], v[52:53]
	ds_bpermute_b32 v53, v34, v49
	ds_bpermute_b32 v52, v34, v48
	s_waitcnt lgkmcnt(2)
	v_pk_add_f32 v[40:41], v[40:41], v[50:51]
	ds_bpermute_b32 v51, v35, v41
	ds_bpermute_b32 v50, v35, v40
	v_mul_f32_e32 v39, 0xbfb8aa3b, v39
	s_waitcnt lgkmcnt(2)
	v_pk_add_f32 v[48:49], v[48:49], v[52:53]
	ds_bpermute_b32 v53, v35, v49
	ds_bpermute_b32 v52, v35, v48
	s_waitcnt lgkmcnt(2)
	v_pk_add_f32 v[40:41], v[40:41], v[50:51]
	ds_bpermute_b32 v51, v36, v41
	ds_bpermute_b32 v50, v36, v40
	v_mul_f32_e32 v62, 0xbfb8aa3b, v76
	s_waitcnt lgkmcnt(2)
	v_pk_add_f32 v[48:49], v[48:49], v[52:53]
	ds_bpermute_b32 v53, v36, v49
	ds_bpermute_b32 v52, v36, v48
	s_waitcnt lgkmcnt(2)
	v_pk_add_f32 v[40:41], v[40:41], v[50:51]
	ds_bpermute_b32 v51, v37, v41
	ds_bpermute_b32 v50, v37, v40
	v_mul_f32_e32 v76, 0xbfb8aa3b, v80
	s_waitcnt lgkmcnt(2)
	v_pk_add_f32 v[48:49], v[48:49], v[52:53]
	ds_bpermute_b32 v53, v37, v49
	ds_bpermute_b32 v52, v37, v48
	s_waitcnt lgkmcnt(2)
	v_pk_add_f32 v[40:41], v[40:41], v[50:51]
	ds_bpermute_b32 v51, v38, v41
	ds_bpermute_b32 v50, v38, v40
	v_exp_f32_e32 v19, v19
	s_waitcnt lgkmcnt(2)
	v_pk_add_f32 v[48:49], v[48:49], v[52:53]
	ds_bpermute_b32 v53, v38, v49
	ds_bpermute_b32 v52, v38, v48
	s_waitcnt lgkmcnt(2)
	v_pk_add_f32 v[40:41], v[40:41], v[50:51]
	v_exp_f32_e32 v39, v39
	v_pk_fma_f32 v[40:41], v[40:41], s[22:23], v[26:27] op_sel_hi:[1,0,0]
	v_exp_f32_e32 v80, v86
	v_mul_f32_e32 v50, 0x4b800000, v41
	v_cmp_gt_f32_e64 s[8:9], s15, v41
	s_waitcnt lgkmcnt(0)
	v_pk_add_f32 v[48:49], v[48:49], v[52:53]
	v_mul_f32_e32 v64, 0xbfb8aa3b, v78
	v_cndmask_b32_e64 v41, v41, v50, s[8:9]
	v_mul_f32_e32 v78, 0xbfb8aa3b, v81
	v_exp_f32_e32 v81, v87
	v_pk_fma_f32 v[48:49], v[48:49], s[22:23], v[26:27] op_sel_hi:[1,0,0]
	v_mul_f32_e32 v51, 0x4b800000, v40
	v_cmp_gt_f32_e32 vcc, s15, v40
	v_rsq_f32_e32 v41, v41
	v_exp_f32_e32 v60, v62
	v_exp_f32_e32 v61, v63
	v_exp_f32_e32 v62, v64
	v_exp_f32_e32 v63, v65
	v_mul_f32_e32 v52, 0x4b800000, v49
	v_mul_f32_e32 v53, 0x4b800000, v48
	v_cmp_gt_f32_e64 s[4:5], s15, v48
	v_cmp_gt_f32_e64 s[6:7], s15, v49
	v_cndmask_b32_e32 v40, v40, v51, vcc
	v_mul_f32_e32 v70, 0xbfb8aa3b, v82
	v_mul_f32_e32 v71, 0xbfb8aa3b, v83
	v_mul_f32_e32 v72, 0xbfb8aa3b, v84
	v_mul_f32_e32 v73, 0xbfb8aa3b, v85
	v_exp_f32_e32 v64, v76
	v_exp_f32_e32 v65, v77
	v_exp_f32_e32 v76, v78
	v_exp_f32_e32 v77, v79
	v_cndmask_b32_e64 v49, v49, v52, s[6:7]
	v_cndmask_b32_e64 v48, v48, v53, s[4:5]
	v_rsq_f32_e32 v40, v40
	v_exp_f32_e32 v68, v70
	v_exp_f32_e32 v69, v71
	v_exp_f32_e32 v70, v72
	v_exp_f32_e32 v71, v73
	v_add_f32_e32 v19, 1.0, v19
	v_add_f32_e32 v39, 1.0, v39
	v_add_f32_e32 v66, 1.0, v80
	v_rsq_f32_e32 v49, v49
	v_rsq_f32_e32 v48, v48
	v_add_f32_e32 v67, 1.0, v81
	v_rcp_f32_e32 v19, v19
	v_rcp_f32_e32 v39, v39
	v_rcp_f32_e32 v66, v66
	v_mul_f32_e32 v50, 0x45800000, v41
	v_add_f32_e32 v60, 1.0, v60
	v_add_f32_e32 v61, 1.0, v61
	v_add_f32_e32 v62, 1.0, v62
	v_add_f32_e32 v63, 1.0, v63
	v_rcp_f32_e32 v67, v67
	v_cndmask_b32_e64 v41, v41, v50, s[8:9]
	v_add_f32_e32 v64, 1.0, v64
	v_add_f32_e32 v65, 1.0, v65
	v_add_f32_e32 v72, 1.0, v76
	v_add_f32_e32 v73, 1.0, v77
	v_rcp_f32_e32 v60, v60
	v_rcp_f32_e32 v61, v61
	v_rcp_f32_e32 v62, v62
	v_rcp_f32_e32 v63, v63
	v_mul_f32_e32 v51, 0x45800000, v40
	v_mul_f32_e32 v28, v41, v28
	v_mul_f32_e32 v29, v41, v29
	v_mul_f32_e32 v31, v41, v31
	v_add_f32_e32 v68, 1.0, v68
	v_add_f32_e32 v69, 1.0, v69
	v_add_f32_e32 v70, 1.0, v70
	v_add_f32_e32 v71, 1.0, v71
	v_rcp_f32_e32 v64, v64
	v_rcp_f32_e32 v65, v65
	v_rcp_f32_e32 v72, v72
	v_rcp_f32_e32 v73, v73
	v_mul_f32_e32 v52, 0x45800000, v49
	v_mul_f32_e32 v53, 0x45800000, v48
	v_cndmask_b32_e32 v40, v40, v51, vcc
	v_mul_f32_e32 v30, v41, v30
	v_mul_f32_e32 v28, v14, v28
	v_mul_f32_e32 v29, v15, v29
	v_mul_f32_e32 v31, v16, v31
	v_rcp_f32_e32 v68, v68
	v_rcp_f32_e32 v69, v69
	v_rcp_f32_e32 v70, v70
	v_rcp_f32_e32 v71, v71
	v_cndmask_b32_e64 v49, v49, v52, s[6:7]
	v_cndmask_b32_e64 v48, v48, v53, s[4:5]
	v_mul_f32_e32 v41, v40, v54
	v_mul_f32_e32 v50, v40, v55
	v_mul_f32_e32 v43, v40, v43
	v_mul_f32_e32 v40, v40, v42
	v_mul_f32_e32 v30, v17, v30
	v_mul_f32_e32 v19, v19, v28
	v_mul_f32_e32 v28, v39, v29
	v_mul_f32_e32 v29, v66, v31
	v_mul_f32_e32 v42, v49, v56
	v_mul_f32_e32 v51, v49, v57
	v_mul_f32_e32 v45, v49, v45
	v_mul_f32_e32 v44, v49, v44
	v_mul_f32_e32 v49, v48, v58
	v_mul_f32_e32 v52, v48, v59
	v_mul_f32_e32 v47, v48, v47
	v_mul_f32_e32 v46, v48, v46
	v_mul_f32_e32 v41, v10, v41
	v_mul_f32_e32 v48, v11, v50
	v_mul_f32_e32 v43, v12, v43
	v_mul_f32_e32 v40, v13, v40
	v_mul_f32_e32 v30, v67, v30
	v_cvt_pk_bf16_f32 v28, v19, v28
	v_cvt_pk_bf16_f32 v29, v29, v30
	v_mul_f32_e32 v42, v6, v42
	v_mul_f32_e32 v50, v7, v51
	v_mul_f32_e32 v45, v8, v45
	v_mul_f32_e32 v44, v9, v44
	v_mul_f32_e32 v31, v60, v41
	v_mul_f32_e32 v39, v61, v48
	v_mul_f32_e32 v41, v62, v43
	v_mul_f32_e32 v40, v63, v40
	global_store_dwordx2 v[32:33], v[28:29], off
	v_cvt_pk_bf16_f32 v28, v31, v39
	v_cvt_pk_bf16_f32 v29, v41, v40
	v_mul_f32_e32 v49, v2, v49
	v_mul_f32_e32 v51, v3, v52
	v_mul_f32_e32 v47, v4, v47
	v_mul_f32_e32 v46, v5, v46
	v_mul_f32_e32 v42, v64, v42
	v_mul_f32_e32 v43, v65, v50
	v_mul_f32_e32 v45, v72, v45
	v_mul_f32_e32 v44, v73, v44
	global_store_dwordx2 v[32:33], v[28:29], off offset:512
	v_cvt_pk_bf16_f32 v28, v42, v43
	v_cvt_pk_bf16_f32 v29, v45, v44
	v_mul_f32_e32 v48, v68, v49
	v_mul_f32_e32 v49, v69, v51
	v_mul_f32_e32 v47, v70, v47
	v_mul_f32_e32 v46, v71, v46
	global_store_dwordx2 v[32:33], v[28:29], off offset:1024
	v_cvt_pk_bf16_f32 v28, v48, v49
	v_cvt_pk_bf16_f32 v29, v47, v46
	global_store_dwordx2 v[32:33], v[28:29], off offset:1536
	s_andn2_b64 exec, exec, s[20:21]
	s_nop 0
	v_lshl_add_u64 v[30:31], v[24:25], 0, v[20:21]
	v_add_co_u32_e32 v40, vcc, 0x3ec4a000, v30
	v_lshl_add_u64 v[28:29], v[22:23], 0, v[20:21]
	v_add_co_u32_e64 v32, s[4:5], s23, v30
	v_addc_co_u32_e32 v41, vcc, 0, v31, vcc
	s_nop 0
	v_addc_co_u32_e64 v33, s[4:5], 0, v31, s[4:5]
	v_add_co_u32_e32 v28, vcc, 0x42c4b000, v28
	s_waitcnt vmcnt(16)
	v_mov_b32_e32 v30, v128
	v_mov_b32_e32 v31, v129
	v_mov_b32_e32 v42, v130
	v_mov_b32_e32 v43, v131
	v_mov_b32_e32 v44, v132
	v_mov_b32_e32 v45, v133
	v_mov_b32_e32 v46, v134
	v_mov_b32_e32 v47, v135
	v_mov_b32_e32 v40, v136
	v_mov_b32_e32 v41, v137
	v_mov_b32_e32 v48, v138
	v_mov_b32_e32 v49, v139
	v_mov_b32_e32 v50, v140
	v_mov_b32_e32 v51, v141
	v_mov_b32_e32 v52, v142
	v_mov_b32_e32 v53, v143
	global_load_dwordx2 v[96:97], v[228:229], off
	global_load_dwordx2 v[98:99], v[228:229], off offset:512
	global_load_dwordx2 v[100:101], v[228:229], off offset:1024
	global_load_dwordx2 v[102:103], v[228:229], off offset:1536
	global_load_dwordx2 v[104:105], v[230:231], off offset:2048
	global_load_dwordx2 v[106:107], v[230:231], off offset:2560
	global_load_dwordx2 v[108:109], v[230:231], off offset:3072
	global_load_dwordx2 v[110:111], v[230:231], off offset:3584
	v_lshl_add_u64 v[228:229], v[228:229], 0, s[18:19]
	v_lshl_add_u64 v[230:231], v[230:231], 0, s[16:17]
	v_addc_co_u32_e32 v29, vcc, 0, v29, vcc
	v_add_u32_e32 v18, s14, v18
	v_cmp_lt_i32_e64 s[4:5], s24, v18
	s_or_b64 s[20:21], s[4:5], s[20:21]
	v_lshl_add_u64 v[22:23], v[22:23], 0, s[16:17]
	v_lshl_add_u64 v[24:25], v[24:25], 0, s[18:19]
	s_nop 0
	v_lshlrev_b32_e32 v28, 16, v30
	v_and_b32_e32 v29, 0xffff0000, v30
	s_nop 0
	v_lshlrev_b32_e32 v54, 16, v42
	v_and_b32_e32 v55, 0xffff0000, v42
	v_and_b32_e32 v30, 0xffff0000, v31
	v_lshlrev_b32_e32 v31, 16, v31
	v_and_b32_e32 v42, 0xffff0000, v43
	v_lshlrev_b32_e32 v43, 16, v43
	v_pk_mul_f32 v[60:61], v[28:29], v[28:29]
	v_pk_mul_f32 v[64:65], v[54:55], v[54:55]
	s_nop 0
	v_lshlrev_b32_e32 v19, 16, v40
	v_and_b32_e32 v39, 0xffff0000, v40
	v_lshlrev_b32_e32 v40, 16, v41
	v_and_b32_e32 v41, 0xffff0000, v41
	v_lshlrev_b32_e32 v56, 16, v44
	v_and_b32_e32 v57, 0xffff0000, v44
	v_lshlrev_b32_e32 v58, 16, v46
	v_and_b32_e32 v59, 0xffff0000, v46
	v_pk_mul_f32 v[62:63], v[30:31], v[30:31]
	v_pk_mul_f32 v[66:67], v[42:43], v[42:43]
	v_mul_f32_e32 v86, 0xbfb8aa3b, v40
	v_mul_f32_e32 v87, 0xbfb8aa3b, v41
	v_mov_b32_e32 v40, v64
	v_mov_b32_e32 v41, v60
	v_mov_b32_e32 v60, v65
	v_and_b32_e32 v44, 0xffff0000, v45
	v_lshlrev_b32_e32 v45, 16, v45
	v_and_b32_e32 v46, 0xffff0000, v47
	v_lshlrev_b32_e32 v47, 16, v47
	v_pk_mul_f32 v[68:69], v[56:57], v[56:57]
	v_pk_mul_f32 v[72:73], v[58:59], v[58:59]
	s_nop 0
	v_lshlrev_b32_e32 v76, 16, v48
	v_and_b32_e32 v77, 0xffff0000, v48
	v_lshlrev_b32_e32 v78, 16, v49
	v_and_b32_e32 v79, 0xffff0000, v49
	s_nop 0
	v_lshlrev_b32_e32 v80, 16, v50
	v_and_b32_e32 v50, 0xffff0000, v50
	v_lshlrev_b32_e32 v81, 16, v51
	v_and_b32_e32 v51, 0xffff0000, v51
	v_mov_b32_e32 v48, v67
	v_mov_b32_e32 v49, v63
	v_pk_add_f32 v[40:41], v[40:41], v[60:61]
	v_pk_mul_f32 v[70:71], v[44:45], v[44:45]
	v_pk_mul_f32 v[74:75], v[46:47], v[46:47]
	v_mov_b32_e32 v67, v62
	v_mul_f32_e32 v63, 0xbfb8aa3b, v77
	v_mul_f32_e32 v65, 0xbfb8aa3b, v79
	v_mul_f32_e32 v77, 0xbfb8aa3b, v50
	v_mul_f32_e32 v79, 0xbfb8aa3b, v51
	v_mov_b32_e32 v50, v72
	v_mov_b32_e32 v51, v68
	v_mov_b32_e32 v68, v73
	v_pk_add_f32 v[40:41], v[48:49], v[40:41]
	s_nop 0
	v_lshlrev_b32_e32 v82, 16, v52
	v_and_b32_e32 v83, 0xffff0000, v52
	v_lshlrev_b32_e32 v84, 16, v53
	v_and_b32_e32 v85, 0xffff0000, v53
	v_mov_b32_e32 v52, v75
	v_mov_b32_e32 v53, v71
	v_pk_add_f32 v[50:51], v[50:51], v[68:69]
	v_pk_add_f32 v[40:41], v[66:67], v[40:41]
	v_pk_add_f32 v[48:49], v[52:53], v[50:51]
	ds_bpermute_b32 v51, v1, v41
	ds_bpermute_b32 v50, v1, v40
	v_mov_b32_e32 v75, v70
	v_pk_add_f32 v[48:49], v[74:75], v[48:49]
	ds_bpermute_b32 v53, v1, v49
	ds_bpermute_b32 v52, v1, v48
	s_waitcnt lgkmcnt(2)
	v_pk_add_f32 v[40:41], v[40:41], v[50:51]
	ds_bpermute_b32 v51, v34, v41
	ds_bpermute_b32 v50, v34, v40
	v_mul_f32_e32 v19, 0xbfb8aa3b, v19
	s_waitcnt lgkmcnt(2)
	v_pk_add_f32 v[48:49], v[48:49], v[52:53]
	ds_bpermute_b32 v53, v34, v49
	ds_bpermute_b32 v52, v34, v48
	s_waitcnt lgkmcnt(2)
	v_pk_add_f32 v[40:41], v[40:41], v[50:51]
	ds_bpermute_b32 v51, v35, v41
	ds_bpermute_b32 v50, v35, v40
	v_mul_f32_e32 v39, 0xbfb8aa3b, v39
	s_waitcnt lgkmcnt(2)
	v_pk_add_f32 v[48:49], v[48:49], v[52:53]
	ds_bpermute_b32 v53, v35, v49
	ds_bpermute_b32 v52, v35, v48
	s_waitcnt lgkmcnt(2)
	v_pk_add_f32 v[40:41], v[40:41], v[50:51]
	ds_bpermute_b32 v51, v36, v41
	ds_bpermute_b32 v50, v36, v40
	v_mul_f32_e32 v62, 0xbfb8aa3b, v76
	s_waitcnt lgkmcnt(2)
	v_pk_add_f32 v[48:49], v[48:49], v[52:53]
	ds_bpermute_b32 v53, v36, v49
	ds_bpermute_b32 v52, v36, v48
	s_waitcnt lgkmcnt(2)
	v_pk_add_f32 v[40:41], v[40:41], v[50:51]
	ds_bpermute_b32 v51, v37, v41
	ds_bpermute_b32 v50, v37, v40
	v_mul_f32_e32 v76, 0xbfb8aa3b, v80
	s_waitcnt lgkmcnt(2)
	v_pk_add_f32 v[48:49], v[48:49], v[52:53]
	ds_bpermute_b32 v53, v37, v49
	ds_bpermute_b32 v52, v37, v48
	s_waitcnt lgkmcnt(2)
	v_pk_add_f32 v[40:41], v[40:41], v[50:51]
	ds_bpermute_b32 v51, v38, v41
	ds_bpermute_b32 v50, v38, v40
	v_exp_f32_e32 v19, v19
	s_waitcnt lgkmcnt(2)
	v_pk_add_f32 v[48:49], v[48:49], v[52:53]
	ds_bpermute_b32 v53, v38, v49
	ds_bpermute_b32 v52, v38, v48
	s_waitcnt lgkmcnt(2)
	v_pk_add_f32 v[40:41], v[40:41], v[50:51]
	v_exp_f32_e32 v39, v39
	v_pk_fma_f32 v[40:41], v[40:41], s[22:23], v[26:27] op_sel_hi:[1,0,0]
	v_exp_f32_e32 v80, v86
	v_mul_f32_e32 v50, 0x4b800000, v41
	v_cmp_gt_f32_e64 s[8:9], s15, v41
	s_waitcnt lgkmcnt(0)
	v_pk_add_f32 v[48:49], v[48:49], v[52:53]
	v_mul_f32_e32 v64, 0xbfb8aa3b, v78
	v_cndmask_b32_e64 v41, v41, v50, s[8:9]
	v_mul_f32_e32 v78, 0xbfb8aa3b, v81
	v_exp_f32_e32 v81, v87
	v_pk_fma_f32 v[48:49], v[48:49], s[22:23], v[26:27] op_sel_hi:[1,0,0]
	v_mul_f32_e32 v51, 0x4b800000, v40
	v_cmp_gt_f32_e32 vcc, s15, v40
	v_rsq_f32_e32 v41, v41
	v_exp_f32_e32 v60, v62
	v_exp_f32_e32 v61, v63
	v_exp_f32_e32 v62, v64
	v_exp_f32_e32 v63, v65
	v_mul_f32_e32 v52, 0x4b800000, v49
	v_mul_f32_e32 v53, 0x4b800000, v48
	v_cmp_gt_f32_e64 s[4:5], s15, v48
	v_cmp_gt_f32_e64 s[6:7], s15, v49
	v_cndmask_b32_e32 v40, v40, v51, vcc
	v_mul_f32_e32 v70, 0xbfb8aa3b, v82
	v_mul_f32_e32 v71, 0xbfb8aa3b, v83
	v_mul_f32_e32 v72, 0xbfb8aa3b, v84
	v_mul_f32_e32 v73, 0xbfb8aa3b, v85
	v_exp_f32_e32 v64, v76
	v_exp_f32_e32 v65, v77
	v_exp_f32_e32 v76, v78
	v_exp_f32_e32 v77, v79
	v_cndmask_b32_e64 v49, v49, v52, s[6:7]
	v_cndmask_b32_e64 v48, v48, v53, s[4:5]
	v_rsq_f32_e32 v40, v40
	v_exp_f32_e32 v68, v70
	v_exp_f32_e32 v69, v71
	v_exp_f32_e32 v70, v72
	v_exp_f32_e32 v71, v73
	v_add_f32_e32 v19, 1.0, v19
	v_add_f32_e32 v39, 1.0, v39
	v_add_f32_e32 v66, 1.0, v80
	v_rsq_f32_e32 v49, v49
	v_rsq_f32_e32 v48, v48
	v_add_f32_e32 v67, 1.0, v81
	v_rcp_f32_e32 v19, v19
	v_rcp_f32_e32 v39, v39
	v_rcp_f32_e32 v66, v66
	v_mul_f32_e32 v50, 0x45800000, v41
	v_add_f32_e32 v60, 1.0, v60
	v_add_f32_e32 v61, 1.0, v61
	v_add_f32_e32 v62, 1.0, v62
	v_add_f32_e32 v63, 1.0, v63
	v_rcp_f32_e32 v67, v67
	v_cndmask_b32_e64 v41, v41, v50, s[8:9]
	v_add_f32_e32 v64, 1.0, v64
	v_add_f32_e32 v65, 1.0, v65
	v_add_f32_e32 v72, 1.0, v76
	v_add_f32_e32 v73, 1.0, v77
	v_rcp_f32_e32 v60, v60
	v_rcp_f32_e32 v61, v61
	v_rcp_f32_e32 v62, v62
	v_rcp_f32_e32 v63, v63
	v_mul_f32_e32 v51, 0x45800000, v40
	v_mul_f32_e32 v28, v41, v28
	v_mul_f32_e32 v29, v41, v29
	v_mul_f32_e32 v31, v41, v31
	v_add_f32_e32 v68, 1.0, v68
	v_add_f32_e32 v69, 1.0, v69
	v_add_f32_e32 v70, 1.0, v70
	v_add_f32_e32 v71, 1.0, v71
	v_rcp_f32_e32 v64, v64
	v_rcp_f32_e32 v65, v65
	v_rcp_f32_e32 v72, v72
	v_rcp_f32_e32 v73, v73
	v_mul_f32_e32 v52, 0x45800000, v49
	v_mul_f32_e32 v53, 0x45800000, v48
	v_cndmask_b32_e32 v40, v40, v51, vcc
	v_mul_f32_e32 v30, v41, v30
	v_mul_f32_e32 v28, v14, v28
	v_mul_f32_e32 v29, v15, v29
	v_mul_f32_e32 v31, v16, v31
	v_rcp_f32_e32 v68, v68
	v_rcp_f32_e32 v69, v69
	v_rcp_f32_e32 v70, v70
	v_rcp_f32_e32 v71, v71
	v_cndmask_b32_e64 v49, v49, v52, s[6:7]
	v_cndmask_b32_e64 v48, v48, v53, s[4:5]
	v_mul_f32_e32 v41, v40, v54
	v_mul_f32_e32 v50, v40, v55
	v_mul_f32_e32 v43, v40, v43
	v_mul_f32_e32 v40, v40, v42
	v_mul_f32_e32 v30, v17, v30
	v_mul_f32_e32 v19, v19, v28
	v_mul_f32_e32 v28, v39, v29
	v_mul_f32_e32 v29, v66, v31
	v_mul_f32_e32 v42, v49, v56
	v_mul_f32_e32 v51, v49, v57
	v_mul_f32_e32 v45, v49, v45
	v_mul_f32_e32 v44, v49, v44
	v_mul_f32_e32 v49, v48, v58
	v_mul_f32_e32 v52, v48, v59
	v_mul_f32_e32 v47, v48, v47
	v_mul_f32_e32 v46, v48, v46
	v_mul_f32_e32 v41, v10, v41
	v_mul_f32_e32 v48, v11, v50
	v_mul_f32_e32 v43, v12, v43
	v_mul_f32_e32 v40, v13, v40
	v_mul_f32_e32 v30, v67, v30
	v_cvt_pk_bf16_f32 v28, v19, v28
	v_cvt_pk_bf16_f32 v29, v29, v30
	v_mul_f32_e32 v42, v6, v42
	v_mul_f32_e32 v50, v7, v51
	v_mul_f32_e32 v45, v8, v45
	v_mul_f32_e32 v44, v9, v44
	v_mul_f32_e32 v31, v60, v41
	v_mul_f32_e32 v39, v61, v48
	v_mul_f32_e32 v41, v62, v43
	v_mul_f32_e32 v40, v63, v40
	global_store_dwordx2 v[32:33], v[28:29], off
	v_cvt_pk_bf16_f32 v28, v31, v39
	v_cvt_pk_bf16_f32 v29, v41, v40
	v_mul_f32_e32 v49, v2, v49
	v_mul_f32_e32 v51, v3, v52
	v_mul_f32_e32 v47, v4, v47
	v_mul_f32_e32 v46, v5, v46
	v_mul_f32_e32 v42, v64, v42
	v_mul_f32_e32 v43, v65, v50
	v_mul_f32_e32 v45, v72, v45
	v_mul_f32_e32 v44, v73, v44
	global_store_dwordx2 v[32:33], v[28:29], off offset:512
	v_cvt_pk_bf16_f32 v28, v42, v43
	v_cvt_pk_bf16_f32 v29, v45, v44
	v_mul_f32_e32 v48, v68, v49
	v_mul_f32_e32 v49, v69, v51
	v_mul_f32_e32 v47, v70, v47
	v_mul_f32_e32 v46, v71, v46
	global_store_dwordx2 v[32:33], v[28:29], off offset:1024
	v_cvt_pk_bf16_f32 v28, v48, v49
	v_cvt_pk_bf16_f32 v29, v47, v46
	global_store_dwordx2 v[32:33], v[28:29], off offset:1536
	s_andn2_b64 exec, exec, s[20:21]
	s_nop 0
	v_lshl_add_u64 v[30:31], v[24:25], 0, v[20:21]
	v_add_co_u32_e32 v40, vcc, 0x3ec4a000, v30
	v_lshl_add_u64 v[28:29], v[22:23], 0, v[20:21]
	v_add_co_u32_e64 v32, s[4:5], s23, v30
	v_addc_co_u32_e32 v41, vcc, 0, v31, vcc
	s_nop 0
	v_addc_co_u32_e64 v33, s[4:5], 0, v31, s[4:5]
	v_add_co_u32_e32 v28, vcc, 0x42c4b000, v28
	s_waitcnt vmcnt(16)
	v_mov_b32_e32 v30, v144
	v_mov_b32_e32 v31, v145
	v_mov_b32_e32 v42, v146
	v_mov_b32_e32 v43, v147
	v_mov_b32_e32 v44, v148
	v_mov_b32_e32 v45, v149
	v_mov_b32_e32 v46, v150
	v_mov_b32_e32 v47, v151
	v_mov_b32_e32 v40, v152
	v_mov_b32_e32 v41, v153
	v_mov_b32_e32 v48, v154
	v_mov_b32_e32 v49, v155
	v_mov_b32_e32 v50, v156
	v_mov_b32_e32 v51, v157
	v_mov_b32_e32 v52, v158
	v_mov_b32_e32 v53, v159
	global_load_dwordx2 v[112:113], v[228:229], off
	global_load_dwordx2 v[114:115], v[228:229], off offset:512
	global_load_dwordx2 v[116:117], v[228:229], off offset:1024
	global_load_dwordx2 v[118:119], v[228:229], off offset:1536
	global_load_dwordx2 v[120:121], v[230:231], off offset:2048
	global_load_dwordx2 v[122:123], v[230:231], off offset:2560
	global_load_dwordx2 v[124:125], v[230:231], off offset:3072
	global_load_dwordx2 v[126:127], v[230:231], off offset:3584
	v_lshl_add_u64 v[228:229], v[228:229], 0, s[18:19]
	v_lshl_add_u64 v[230:231], v[230:231], 0, s[16:17]
	v_addc_co_u32_e32 v29, vcc, 0, v29, vcc
	v_add_u32_e32 v18, s14, v18
	v_cmp_lt_i32_e64 s[4:5], s24, v18
	s_or_b64 s[20:21], s[4:5], s[20:21]
	v_lshl_add_u64 v[22:23], v[22:23], 0, s[16:17]
	v_lshl_add_u64 v[24:25], v[24:25], 0, s[18:19]
	s_nop 0
	v_lshlrev_b32_e32 v28, 16, v30
	v_and_b32_e32 v29, 0xffff0000, v30
	s_nop 0
	v_lshlrev_b32_e32 v54, 16, v42
	v_and_b32_e32 v55, 0xffff0000, v42
	v_and_b32_e32 v30, 0xffff0000, v31
	v_lshlrev_b32_e32 v31, 16, v31
	v_and_b32_e32 v42, 0xffff0000, v43
	v_lshlrev_b32_e32 v43, 16, v43
	v_pk_mul_f32 v[60:61], v[28:29], v[28:29]
	v_pk_mul_f32 v[64:65], v[54:55], v[54:55]
	s_nop 0
	v_lshlrev_b32_e32 v19, 16, v40
	v_and_b32_e32 v39, 0xffff0000, v40
	v_lshlrev_b32_e32 v40, 16, v41
	v_and_b32_e32 v41, 0xffff0000, v41
	v_lshlrev_b32_e32 v56, 16, v44
	v_and_b32_e32 v57, 0xffff0000, v44
	v_lshlrev_b32_e32 v58, 16, v46
	v_and_b32_e32 v59, 0xffff0000, v46
	v_pk_mul_f32 v[62:63], v[30:31], v[30:31]
	v_pk_mul_f32 v[66:67], v[42:43], v[42:43]
	v_mul_f32_e32 v86, 0xbfb8aa3b, v40
	v_mul_f32_e32 v87, 0xbfb8aa3b, v41
	v_mov_b32_e32 v40, v64
	v_mov_b32_e32 v41, v60
	v_mov_b32_e32 v60, v65
	v_and_b32_e32 v44, 0xffff0000, v45
	v_lshlrev_b32_e32 v45, 16, v45
	v_and_b32_e32 v46, 0xffff0000, v47
	v_lshlrev_b32_e32 v47, 16, v47
	v_pk_mul_f32 v[68:69], v[56:57], v[56:57]
	v_pk_mul_f32 v[72:73], v[58:59], v[58:59]
	s_nop 0
	v_lshlrev_b32_e32 v76, 16, v48
	v_and_b32_e32 v77, 0xffff0000, v48
	v_lshlrev_b32_e32 v78, 16, v49
	v_and_b32_e32 v79, 0xffff0000, v49
	s_nop 0
	v_lshlrev_b32_e32 v80, 16, v50
	v_and_b32_e32 v50, 0xffff0000, v50
	v_lshlrev_b32_e32 v81, 16, v51
	v_and_b32_e32 v51, 0xffff0000, v51
	v_mov_b32_e32 v48, v67
	v_mov_b32_e32 v49, v63
	v_pk_add_f32 v[40:41], v[40:41], v[60:61]
	v_pk_mul_f32 v[70:71], v[44:45], v[44:45]
	v_pk_mul_f32 v[74:75], v[46:47], v[46:47]
	v_mov_b32_e32 v67, v62
	v_mul_f32_e32 v63, 0xbfb8aa3b, v77
	v_mul_f32_e32 v65, 0xbfb8aa3b, v79
	v_mul_f32_e32 v77, 0xbfb8aa3b, v50
	v_mul_f32_e32 v79, 0xbfb8aa3b, v51
	v_mov_b32_e32 v50, v72
	v_mov_b32_e32 v51, v68
	v_mov_b32_e32 v68, v73
	v_pk_add_f32 v[40:41], v[48:49], v[40:41]
	s_nop 0
	v_lshlrev_b32_e32 v82, 16, v52
	v_and_b32_e32 v83, 0xffff0000, v52
	v_lshlrev_b32_e32 v84, 16, v53
	v_and_b32_e32 v85, 0xffff0000, v53
	v_mov_b32_e32 v52, v75
	v_mov_b32_e32 v53, v71
	v_pk_add_f32 v[50:51], v[50:51], v[68:69]
	v_pk_add_f32 v[40:41], v[66:67], v[40:41]
	v_pk_add_f32 v[48:49], v[52:53], v[50:51]
	ds_bpermute_b32 v51, v1, v41
	ds_bpermute_b32 v50, v1, v40
	v_mov_b32_e32 v75, v70
	v_pk_add_f32 v[48:49], v[74:75], v[48:49]
	ds_bpermute_b32 v53, v1, v49
	ds_bpermute_b32 v52, v1, v48
	s_waitcnt lgkmcnt(2)
	v_pk_add_f32 v[40:41], v[40:41], v[50:51]
	ds_bpermute_b32 v51, v34, v41
	ds_bpermute_b32 v50, v34, v40
	v_mul_f32_e32 v19, 0xbfb8aa3b, v19
	s_waitcnt lgkmcnt(2)
	v_pk_add_f32 v[48:49], v[48:49], v[52:53]
	ds_bpermute_b32 v53, v34, v49
	ds_bpermute_b32 v52, v34, v48
	s_waitcnt lgkmcnt(2)
	v_pk_add_f32 v[40:41], v[40:41], v[50:51]
	ds_bpermute_b32 v51, v35, v41
	ds_bpermute_b32 v50, v35, v40
	v_mul_f32_e32 v39, 0xbfb8aa3b, v39
	s_waitcnt lgkmcnt(2)
	v_pk_add_f32 v[48:49], v[48:49], v[52:53]
	ds_bpermute_b32 v53, v35, v49
	ds_bpermute_b32 v52, v35, v48
	s_waitcnt lgkmcnt(2)
	v_pk_add_f32 v[40:41], v[40:41], v[50:51]
	ds_bpermute_b32 v51, v36, v41
	ds_bpermute_b32 v50, v36, v40
	v_mul_f32_e32 v62, 0xbfb8aa3b, v76
	s_waitcnt lgkmcnt(2)
	v_pk_add_f32 v[48:49], v[48:49], v[52:53]
	ds_bpermute_b32 v53, v36, v49
	ds_bpermute_b32 v52, v36, v48
	s_waitcnt lgkmcnt(2)
	v_pk_add_f32 v[40:41], v[40:41], v[50:51]
	ds_bpermute_b32 v51, v37, v41
	ds_bpermute_b32 v50, v37, v40
	v_mul_f32_e32 v76, 0xbfb8aa3b, v80
	s_waitcnt lgkmcnt(2)
	v_pk_add_f32 v[48:49], v[48:49], v[52:53]
	ds_bpermute_b32 v53, v37, v49
	ds_bpermute_b32 v52, v37, v48
	s_waitcnt lgkmcnt(2)
	v_pk_add_f32 v[40:41], v[40:41], v[50:51]
	ds_bpermute_b32 v51, v38, v41
	ds_bpermute_b32 v50, v38, v40
	v_exp_f32_e32 v19, v19
	s_waitcnt lgkmcnt(2)
	v_pk_add_f32 v[48:49], v[48:49], v[52:53]
	ds_bpermute_b32 v53, v38, v49
	ds_bpermute_b32 v52, v38, v48
	s_waitcnt lgkmcnt(2)
	v_pk_add_f32 v[40:41], v[40:41], v[50:51]
	v_exp_f32_e32 v39, v39
	v_pk_fma_f32 v[40:41], v[40:41], s[22:23], v[26:27] op_sel_hi:[1,0,0]
	v_exp_f32_e32 v80, v86
	v_mul_f32_e32 v50, 0x4b800000, v41
	v_cmp_gt_f32_e64 s[8:9], s15, v41
	s_waitcnt lgkmcnt(0)
	v_pk_add_f32 v[48:49], v[48:49], v[52:53]
	v_mul_f32_e32 v64, 0xbfb8aa3b, v78
	v_cndmask_b32_e64 v41, v41, v50, s[8:9]
	v_mul_f32_e32 v78, 0xbfb8aa3b, v81
	v_exp_f32_e32 v81, v87
	v_pk_fma_f32 v[48:49], v[48:49], s[22:23], v[26:27] op_sel_hi:[1,0,0]
	v_mul_f32_e32 v51, 0x4b800000, v40
	v_cmp_gt_f32_e32 vcc, s15, v40
	v_rsq_f32_e32 v41, v41
	v_exp_f32_e32 v60, v62
	v_exp_f32_e32 v61, v63
	v_exp_f32_e32 v62, v64
	v_exp_f32_e32 v63, v65
	v_mul_f32_e32 v52, 0x4b800000, v49
	v_mul_f32_e32 v53, 0x4b800000, v48
	v_cmp_gt_f32_e64 s[4:5], s15, v48
	v_cmp_gt_f32_e64 s[6:7], s15, v49
	v_cndmask_b32_e32 v40, v40, v51, vcc
	v_mul_f32_e32 v70, 0xbfb8aa3b, v82
	v_mul_f32_e32 v71, 0xbfb8aa3b, v83
	v_mul_f32_e32 v72, 0xbfb8aa3b, v84
	v_mul_f32_e32 v73, 0xbfb8aa3b, v85
	v_exp_f32_e32 v64, v76
	v_exp_f32_e32 v65, v77
	v_exp_f32_e32 v76, v78
	v_exp_f32_e32 v77, v79
	v_cndmask_b32_e64 v49, v49, v52, s[6:7]
	v_cndmask_b32_e64 v48, v48, v53, s[4:5]
	v_rsq_f32_e32 v40, v40
	v_exp_f32_e32 v68, v70
	v_exp_f32_e32 v69, v71
	v_exp_f32_e32 v70, v72
	v_exp_f32_e32 v71, v73
	v_add_f32_e32 v19, 1.0, v19
	v_add_f32_e32 v39, 1.0, v39
	v_add_f32_e32 v66, 1.0, v80
	v_rsq_f32_e32 v49, v49
	v_rsq_f32_e32 v48, v48
	v_add_f32_e32 v67, 1.0, v81
	v_rcp_f32_e32 v19, v19
	v_rcp_f32_e32 v39, v39
	v_rcp_f32_e32 v66, v66
	v_mul_f32_e32 v50, 0x45800000, v41
	v_add_f32_e32 v60, 1.0, v60
	v_add_f32_e32 v61, 1.0, v61
	v_add_f32_e32 v62, 1.0, v62
	v_add_f32_e32 v63, 1.0, v63
	v_rcp_f32_e32 v67, v67
	v_cndmask_b32_e64 v41, v41, v50, s[8:9]
	v_add_f32_e32 v64, 1.0, v64
	v_add_f32_e32 v65, 1.0, v65
	v_add_f32_e32 v72, 1.0, v76
	v_add_f32_e32 v73, 1.0, v77
	v_rcp_f32_e32 v60, v60
	v_rcp_f32_e32 v61, v61
	v_rcp_f32_e32 v62, v62
	v_rcp_f32_e32 v63, v63
	v_mul_f32_e32 v51, 0x45800000, v40
	v_mul_f32_e32 v28, v41, v28
	v_mul_f32_e32 v29, v41, v29
	v_mul_f32_e32 v31, v41, v31
	v_add_f32_e32 v68, 1.0, v68
	v_add_f32_e32 v69, 1.0, v69
	v_add_f32_e32 v70, 1.0, v70
	v_add_f32_e32 v71, 1.0, v71
	v_rcp_f32_e32 v64, v64
	v_rcp_f32_e32 v65, v65
	v_rcp_f32_e32 v72, v72
	v_rcp_f32_e32 v73, v73
	v_mul_f32_e32 v52, 0x45800000, v49
	v_mul_f32_e32 v53, 0x45800000, v48
	v_cndmask_b32_e32 v40, v40, v51, vcc
	v_mul_f32_e32 v30, v41, v30
	v_mul_f32_e32 v28, v14, v28
	v_mul_f32_e32 v29, v15, v29
	v_mul_f32_e32 v31, v16, v31
	v_rcp_f32_e32 v68, v68
	v_rcp_f32_e32 v69, v69
	v_rcp_f32_e32 v70, v70
	v_rcp_f32_e32 v71, v71
	v_cndmask_b32_e64 v49, v49, v52, s[6:7]
	v_cndmask_b32_e64 v48, v48, v53, s[4:5]
	v_mul_f32_e32 v41, v40, v54
	v_mul_f32_e32 v50, v40, v55
	v_mul_f32_e32 v43, v40, v43
	v_mul_f32_e32 v40, v40, v42
	v_mul_f32_e32 v30, v17, v30
	v_mul_f32_e32 v19, v19, v28
	v_mul_f32_e32 v28, v39, v29
	v_mul_f32_e32 v29, v66, v31
	v_mul_f32_e32 v42, v49, v56
	v_mul_f32_e32 v51, v49, v57
	v_mul_f32_e32 v45, v49, v45
	v_mul_f32_e32 v44, v49, v44
	v_mul_f32_e32 v49, v48, v58
	v_mul_f32_e32 v52, v48, v59
	v_mul_f32_e32 v47, v48, v47
	v_mul_f32_e32 v46, v48, v46
	v_mul_f32_e32 v41, v10, v41
	v_mul_f32_e32 v48, v11, v50
	v_mul_f32_e32 v43, v12, v43
	v_mul_f32_e32 v40, v13, v40
	v_mul_f32_e32 v30, v67, v30
	v_cvt_pk_bf16_f32 v28, v19, v28
	v_cvt_pk_bf16_f32 v29, v29, v30
	v_mul_f32_e32 v42, v6, v42
	v_mul_f32_e32 v50, v7, v51
	v_mul_f32_e32 v45, v8, v45
	v_mul_f32_e32 v44, v9, v44
	v_mul_f32_e32 v31, v60, v41
	v_mul_f32_e32 v39, v61, v48
	v_mul_f32_e32 v41, v62, v43
	v_mul_f32_e32 v40, v63, v40
	global_store_dwordx2 v[32:33], v[28:29], off
	v_cvt_pk_bf16_f32 v28, v31, v39
	v_cvt_pk_bf16_f32 v29, v41, v40
	v_mul_f32_e32 v49, v2, v49
	v_mul_f32_e32 v51, v3, v52
	v_mul_f32_e32 v47, v4, v47
	v_mul_f32_e32 v46, v5, v46
	v_mul_f32_e32 v42, v64, v42
	v_mul_f32_e32 v43, v65, v50
	v_mul_f32_e32 v45, v72, v45
	v_mul_f32_e32 v44, v73, v44
	global_store_dwordx2 v[32:33], v[28:29], off offset:512
	v_cvt_pk_bf16_f32 v28, v42, v43
	v_cvt_pk_bf16_f32 v29, v45, v44
	v_mul_f32_e32 v48, v68, v49
	v_mul_f32_e32 v49, v69, v51
	v_mul_f32_e32 v47, v70, v47
	v_mul_f32_e32 v46, v71, v46
	global_store_dwordx2 v[32:33], v[28:29], off offset:1024
	v_cvt_pk_bf16_f32 v28, v48, v49
	v_cvt_pk_bf16_f32 v29, v47, v46
	global_store_dwordx2 v[32:33], v[28:29], off offset:1536
	s_andn2_b64 exec, exec, s[20:21]
	s_nop 0
	v_lshl_add_u64 v[30:31], v[24:25], 0, v[20:21]
	v_add_co_u32_e32 v40, vcc, 0x3ec4a000, v30
	v_lshl_add_u64 v[28:29], v[22:23], 0, v[20:21]
	v_add_co_u32_e64 v32, s[4:5], s23, v30
	v_addc_co_u32_e32 v41, vcc, 0, v31, vcc
	s_nop 0
	v_addc_co_u32_e64 v33, s[4:5], 0, v31, s[4:5]
	v_add_co_u32_e32 v28, vcc, 0x42c4b000, v28
	s_waitcnt vmcnt(16)
	v_mov_b32_e32 v30, v96
	v_mov_b32_e32 v31, v97
	v_mov_b32_e32 v42, v98
	v_mov_b32_e32 v43, v99
	v_mov_b32_e32 v44, v100
	v_mov_b32_e32 v45, v101
	v_mov_b32_e32 v46, v102
	v_mov_b32_e32 v47, v103
	v_mov_b32_e32 v40, v104
	v_mov_b32_e32 v41, v105
	v_mov_b32_e32 v48, v106
	v_mov_b32_e32 v49, v107
	v_mov_b32_e32 v50, v108
	v_mov_b32_e32 v51, v109
	v_mov_b32_e32 v52, v110
	v_mov_b32_e32 v53, v111
	global_load_dwordx2 v[128:129], v[228:229], off
	global_load_dwordx2 v[130:131], v[228:229], off offset:512
	global_load_dwordx2 v[132:133], v[228:229], off offset:1024
	global_load_dwordx2 v[134:135], v[228:229], off offset:1536
	global_load_dwordx2 v[136:137], v[230:231], off offset:2048
	global_load_dwordx2 v[138:139], v[230:231], off offset:2560
	global_load_dwordx2 v[140:141], v[230:231], off offset:3072
	global_load_dwordx2 v[142:143], v[230:231], off offset:3584
	v_lshl_add_u64 v[228:229], v[228:229], 0, s[18:19]
	v_lshl_add_u64 v[230:231], v[230:231], 0, s[16:17]
	v_addc_co_u32_e32 v29, vcc, 0, v29, vcc
	v_add_u32_e32 v18, s14, v18
	v_cmp_lt_i32_e64 s[4:5], s24, v18
	s_or_b64 s[20:21], s[4:5], s[20:21]
	v_lshl_add_u64 v[22:23], v[22:23], 0, s[16:17]
	v_lshl_add_u64 v[24:25], v[24:25], 0, s[18:19]
	s_nop 0
	v_lshlrev_b32_e32 v28, 16, v30
	v_and_b32_e32 v29, 0xffff0000, v30
	s_nop 0
	v_lshlrev_b32_e32 v54, 16, v42
	v_and_b32_e32 v55, 0xffff0000, v42
	v_and_b32_e32 v30, 0xffff0000, v31
	v_lshlrev_b32_e32 v31, 16, v31
	v_and_b32_e32 v42, 0xffff0000, v43
	v_lshlrev_b32_e32 v43, 16, v43
	v_pk_mul_f32 v[60:61], v[28:29], v[28:29]
	v_pk_mul_f32 v[64:65], v[54:55], v[54:55]
	s_nop 0
	v_lshlrev_b32_e32 v19, 16, v40
	v_and_b32_e32 v39, 0xffff0000, v40
	v_lshlrev_b32_e32 v40, 16, v41
	v_and_b32_e32 v41, 0xffff0000, v41
	v_lshlrev_b32_e32 v56, 16, v44
	v_and_b32_e32 v57, 0xffff0000, v44
	v_lshlrev_b32_e32 v58, 16, v46
	v_and_b32_e32 v59, 0xffff0000, v46
	v_pk_mul_f32 v[62:63], v[30:31], v[30:31]
	v_pk_mul_f32 v[66:67], v[42:43], v[42:43]
	v_mul_f32_e32 v86, 0xbfb8aa3b, v40
	v_mul_f32_e32 v87, 0xbfb8aa3b, v41
	v_mov_b32_e32 v40, v64
	v_mov_b32_e32 v41, v60
	v_mov_b32_e32 v60, v65
	v_and_b32_e32 v44, 0xffff0000, v45
	v_lshlrev_b32_e32 v45, 16, v45
	v_and_b32_e32 v46, 0xffff0000, v47
	v_lshlrev_b32_e32 v47, 16, v47
	v_pk_mul_f32 v[68:69], v[56:57], v[56:57]
	v_pk_mul_f32 v[72:73], v[58:59], v[58:59]
	s_nop 0
	v_lshlrev_b32_e32 v76, 16, v48
	v_and_b32_e32 v77, 0xffff0000, v48
	v_lshlrev_b32_e32 v78, 16, v49
	v_and_b32_e32 v79, 0xffff0000, v49
	s_nop 0
	v_lshlrev_b32_e32 v80, 16, v50
	v_and_b32_e32 v50, 0xffff0000, v50
	v_lshlrev_b32_e32 v81, 16, v51
	v_and_b32_e32 v51, 0xffff0000, v51
	v_mov_b32_e32 v48, v67
	v_mov_b32_e32 v49, v63
	v_pk_add_f32 v[40:41], v[40:41], v[60:61]
	v_pk_mul_f32 v[70:71], v[44:45], v[44:45]
	v_pk_mul_f32 v[74:75], v[46:47], v[46:47]
	v_mov_b32_e32 v67, v62
	v_mul_f32_e32 v63, 0xbfb8aa3b, v77
	v_mul_f32_e32 v65, 0xbfb8aa3b, v79
	v_mul_f32_e32 v77, 0xbfb8aa3b, v50
	v_mul_f32_e32 v79, 0xbfb8aa3b, v51
	v_mov_b32_e32 v50, v72
	v_mov_b32_e32 v51, v68
	v_mov_b32_e32 v68, v73
	v_pk_add_f32 v[40:41], v[48:49], v[40:41]
	s_nop 0
	v_lshlrev_b32_e32 v82, 16, v52
	v_and_b32_e32 v83, 0xffff0000, v52
	v_lshlrev_b32_e32 v84, 16, v53
	v_and_b32_e32 v85, 0xffff0000, v53
	v_mov_b32_e32 v52, v75
	v_mov_b32_e32 v53, v71
	v_pk_add_f32 v[50:51], v[50:51], v[68:69]
	v_pk_add_f32 v[40:41], v[66:67], v[40:41]
	v_pk_add_f32 v[48:49], v[52:53], v[50:51]
	ds_bpermute_b32 v51, v1, v41
	ds_bpermute_b32 v50, v1, v40
	v_mov_b32_e32 v75, v70
	v_pk_add_f32 v[48:49], v[74:75], v[48:49]
	ds_bpermute_b32 v53, v1, v49
	ds_bpermute_b32 v52, v1, v48
	s_waitcnt lgkmcnt(2)
	v_pk_add_f32 v[40:41], v[40:41], v[50:51]
	ds_bpermute_b32 v51, v34, v41
	ds_bpermute_b32 v50, v34, v40
	v_mul_f32_e32 v19, 0xbfb8aa3b, v19
	s_waitcnt lgkmcnt(2)
	v_pk_add_f32 v[48:49], v[48:49], v[52:53]
	ds_bpermute_b32 v53, v34, v49
	ds_bpermute_b32 v52, v34, v48
	s_waitcnt lgkmcnt(2)
	v_pk_add_f32 v[40:41], v[40:41], v[50:51]
	ds_bpermute_b32 v51, v35, v41
	ds_bpermute_b32 v50, v35, v40
	v_mul_f32_e32 v39, 0xbfb8aa3b, v39
	s_waitcnt lgkmcnt(2)
	v_pk_add_f32 v[48:49], v[48:49], v[52:53]
	ds_bpermute_b32 v53, v35, v49
	ds_bpermute_b32 v52, v35, v48
	s_waitcnt lgkmcnt(2)
	v_pk_add_f32 v[40:41], v[40:41], v[50:51]
	ds_bpermute_b32 v51, v36, v41
	ds_bpermute_b32 v50, v36, v40
	v_mul_f32_e32 v62, 0xbfb8aa3b, v76
	s_waitcnt lgkmcnt(2)
	v_pk_add_f32 v[48:49], v[48:49], v[52:53]
	ds_bpermute_b32 v53, v36, v49
	ds_bpermute_b32 v52, v36, v48
	s_waitcnt lgkmcnt(2)
	v_pk_add_f32 v[40:41], v[40:41], v[50:51]
	ds_bpermute_b32 v51, v37, v41
	ds_bpermute_b32 v50, v37, v40
	v_mul_f32_e32 v76, 0xbfb8aa3b, v80
	s_waitcnt lgkmcnt(2)
	v_pk_add_f32 v[48:49], v[48:49], v[52:53]
	ds_bpermute_b32 v53, v37, v49
	ds_bpermute_b32 v52, v37, v48
	s_waitcnt lgkmcnt(2)
	v_pk_add_f32 v[40:41], v[40:41], v[50:51]
	ds_bpermute_b32 v51, v38, v41
	ds_bpermute_b32 v50, v38, v40
	v_exp_f32_e32 v19, v19
	s_waitcnt lgkmcnt(2)
	v_pk_add_f32 v[48:49], v[48:49], v[52:53]
	ds_bpermute_b32 v53, v38, v49
	ds_bpermute_b32 v52, v38, v48
	s_waitcnt lgkmcnt(2)
	v_pk_add_f32 v[40:41], v[40:41], v[50:51]
	v_exp_f32_e32 v39, v39
	v_pk_fma_f32 v[40:41], v[40:41], s[22:23], v[26:27] op_sel_hi:[1,0,0]
	v_exp_f32_e32 v80, v86
	v_mul_f32_e32 v50, 0x4b800000, v41
	v_cmp_gt_f32_e64 s[8:9], s15, v41
	s_waitcnt lgkmcnt(0)
	v_pk_add_f32 v[48:49], v[48:49], v[52:53]
	v_mul_f32_e32 v64, 0xbfb8aa3b, v78
	v_cndmask_b32_e64 v41, v41, v50, s[8:9]
	v_mul_f32_e32 v78, 0xbfb8aa3b, v81
	v_exp_f32_e32 v81, v87
	v_pk_fma_f32 v[48:49], v[48:49], s[22:23], v[26:27] op_sel_hi:[1,0,0]
	v_mul_f32_e32 v51, 0x4b800000, v40
	v_cmp_gt_f32_e32 vcc, s15, v40
	v_rsq_f32_e32 v41, v41
	v_exp_f32_e32 v60, v62
	v_exp_f32_e32 v61, v63
	v_exp_f32_e32 v62, v64
	v_exp_f32_e32 v63, v65
	v_mul_f32_e32 v52, 0x4b800000, v49
	v_mul_f32_e32 v53, 0x4b800000, v48
	v_cmp_gt_f32_e64 s[4:5], s15, v48
	v_cmp_gt_f32_e64 s[6:7], s15, v49
	v_cndmask_b32_e32 v40, v40, v51, vcc
	v_mul_f32_e32 v70, 0xbfb8aa3b, v82
	v_mul_f32_e32 v71, 0xbfb8aa3b, v83
	v_mul_f32_e32 v72, 0xbfb8aa3b, v84
	v_mul_f32_e32 v73, 0xbfb8aa3b, v85
	v_exp_f32_e32 v64, v76
	v_exp_f32_e32 v65, v77
	v_exp_f32_e32 v76, v78
	v_exp_f32_e32 v77, v79
	v_cndmask_b32_e64 v49, v49, v52, s[6:7]
	v_cndmask_b32_e64 v48, v48, v53, s[4:5]
	v_rsq_f32_e32 v40, v40
	v_exp_f32_e32 v68, v70
	v_exp_f32_e32 v69, v71
	v_exp_f32_e32 v70, v72
	v_exp_f32_e32 v71, v73
	v_add_f32_e32 v19, 1.0, v19
	v_add_f32_e32 v39, 1.0, v39
	v_add_f32_e32 v66, 1.0, v80
	v_rsq_f32_e32 v49, v49
	v_rsq_f32_e32 v48, v48
	v_add_f32_e32 v67, 1.0, v81
	v_rcp_f32_e32 v19, v19
	v_rcp_f32_e32 v39, v39
	v_rcp_f32_e32 v66, v66
	v_mul_f32_e32 v50, 0x45800000, v41
	v_add_f32_e32 v60, 1.0, v60
	v_add_f32_e32 v61, 1.0, v61
	v_add_f32_e32 v62, 1.0, v62
	v_add_f32_e32 v63, 1.0, v63
	v_rcp_f32_e32 v67, v67
	v_cndmask_b32_e64 v41, v41, v50, s[8:9]
	v_add_f32_e32 v64, 1.0, v64
	v_add_f32_e32 v65, 1.0, v65
	v_add_f32_e32 v72, 1.0, v76
	v_add_f32_e32 v73, 1.0, v77
	v_rcp_f32_e32 v60, v60
	v_rcp_f32_e32 v61, v61
	v_rcp_f32_e32 v62, v62
	v_rcp_f32_e32 v63, v63
	v_mul_f32_e32 v51, 0x45800000, v40
	v_mul_f32_e32 v28, v41, v28
	v_mul_f32_e32 v29, v41, v29
	v_mul_f32_e32 v31, v41, v31
	v_add_f32_e32 v68, 1.0, v68
	v_add_f32_e32 v69, 1.0, v69
	v_add_f32_e32 v70, 1.0, v70
	v_add_f32_e32 v71, 1.0, v71
	v_rcp_f32_e32 v64, v64
	v_rcp_f32_e32 v65, v65
	v_rcp_f32_e32 v72, v72
	v_rcp_f32_e32 v73, v73
	v_mul_f32_e32 v52, 0x45800000, v49
	v_mul_f32_e32 v53, 0x45800000, v48
	v_cndmask_b32_e32 v40, v40, v51, vcc
	v_mul_f32_e32 v30, v41, v30
	v_mul_f32_e32 v28, v14, v28
	v_mul_f32_e32 v29, v15, v29
	v_mul_f32_e32 v31, v16, v31
	v_rcp_f32_e32 v68, v68
	v_rcp_f32_e32 v69, v69
	v_rcp_f32_e32 v70, v70
	v_rcp_f32_e32 v71, v71
	v_cndmask_b32_e64 v49, v49, v52, s[6:7]
	v_cndmask_b32_e64 v48, v48, v53, s[4:5]
	v_mul_f32_e32 v41, v40, v54
	v_mul_f32_e32 v50, v40, v55
	v_mul_f32_e32 v43, v40, v43
	v_mul_f32_e32 v40, v40, v42
	v_mul_f32_e32 v30, v17, v30
	v_mul_f32_e32 v19, v19, v28
	v_mul_f32_e32 v28, v39, v29
	v_mul_f32_e32 v29, v66, v31
	v_mul_f32_e32 v42, v49, v56
	v_mul_f32_e32 v51, v49, v57
	v_mul_f32_e32 v45, v49, v45
	v_mul_f32_e32 v44, v49, v44
	v_mul_f32_e32 v49, v48, v58
	v_mul_f32_e32 v52, v48, v59
	v_mul_f32_e32 v47, v48, v47
	v_mul_f32_e32 v46, v48, v46
	v_mul_f32_e32 v41, v10, v41
	v_mul_f32_e32 v48, v11, v50
	v_mul_f32_e32 v43, v12, v43
	v_mul_f32_e32 v40, v13, v40
	v_mul_f32_e32 v30, v67, v30
	v_cvt_pk_bf16_f32 v28, v19, v28
	v_cvt_pk_bf16_f32 v29, v29, v30
	v_mul_f32_e32 v42, v6, v42
	v_mul_f32_e32 v50, v7, v51
	v_mul_f32_e32 v45, v8, v45
	v_mul_f32_e32 v44, v9, v44
	v_mul_f32_e32 v31, v60, v41
	v_mul_f32_e32 v39, v61, v48
	v_mul_f32_e32 v41, v62, v43
	v_mul_f32_e32 v40, v63, v40
	global_store_dwordx2 v[32:33], v[28:29], off
	v_cvt_pk_bf16_f32 v28, v31, v39
	v_cvt_pk_bf16_f32 v29, v41, v40
	v_mul_f32_e32 v49, v2, v49
	v_mul_f32_e32 v51, v3, v52
	v_mul_f32_e32 v47, v4, v47
	v_mul_f32_e32 v46, v5, v46
	v_mul_f32_e32 v42, v64, v42
	v_mul_f32_e32 v43, v65, v50
	v_mul_f32_e32 v45, v72, v45
	v_mul_f32_e32 v44, v73, v44
	global_store_dwordx2 v[32:33], v[28:29], off offset:512
	v_cvt_pk_bf16_f32 v28, v42, v43
	v_cvt_pk_bf16_f32 v29, v45, v44
	v_mul_f32_e32 v48, v68, v49
	v_mul_f32_e32 v49, v69, v51
	v_mul_f32_e32 v47, v70, v47
	v_mul_f32_e32 v46, v71, v46
	global_store_dwordx2 v[32:33], v[28:29], off offset:1024
	v_cvt_pk_bf16_f32 v28, v48, v49
	v_cvt_pk_bf16_f32 v29, v47, v46
	global_store_dwordx2 v[32:33], v[28:29], off offset:1536
	s_andn2_b64 exec, exec, s[20:21]
	s_nop 0
	v_lshl_add_u64 v[30:31], v[24:25], 0, v[20:21]
	v_add_co_u32_e32 v40, vcc, 0x3ec4a000, v30
	v_lshl_add_u64 v[28:29], v[22:23], 0, v[20:21]
	v_add_co_u32_e64 v32, s[4:5], s23, v30
	v_addc_co_u32_e32 v41, vcc, 0, v31, vcc
	s_nop 0
	v_addc_co_u32_e64 v33, s[4:5], 0, v31, s[4:5]
	v_add_co_u32_e32 v28, vcc, 0x42c4b000, v28
	s_waitcnt vmcnt(16)
	v_mov_b32_e32 v30, v112
	v_mov_b32_e32 v31, v113
	v_mov_b32_e32 v42, v114
	v_mov_b32_e32 v43, v115
	v_mov_b32_e32 v44, v116
	v_mov_b32_e32 v45, v117
	v_mov_b32_e32 v46, v118
	v_mov_b32_e32 v47, v119
	v_mov_b32_e32 v40, v120
	v_mov_b32_e32 v41, v121
	v_mov_b32_e32 v48, v122
	v_mov_b32_e32 v49, v123
	v_mov_b32_e32 v50, v124
	v_mov_b32_e32 v51, v125
	v_mov_b32_e32 v52, v126
	v_mov_b32_e32 v53, v127
	global_load_dwordx2 v[144:145], v[228:229], off
	global_load_dwordx2 v[146:147], v[228:229], off offset:512
	global_load_dwordx2 v[148:149], v[228:229], off offset:1024
	global_load_dwordx2 v[150:151], v[228:229], off offset:1536
	global_load_dwordx2 v[152:153], v[230:231], off offset:2048
	global_load_dwordx2 v[154:155], v[230:231], off offset:2560
	global_load_dwordx2 v[156:157], v[230:231], off offset:3072
	global_load_dwordx2 v[158:159], v[230:231], off offset:3584
	v_lshl_add_u64 v[228:229], v[228:229], 0, s[18:19]
	v_lshl_add_u64 v[230:231], v[230:231], 0, s[16:17]
	v_addc_co_u32_e32 v29, vcc, 0, v29, vcc
	v_add_u32_e32 v18, s14, v18
	v_cmp_lt_i32_e64 s[4:5], s24, v18
	s_or_b64 s[20:21], s[4:5], s[20:21]
	v_lshl_add_u64 v[22:23], v[22:23], 0, s[16:17]
	v_lshl_add_u64 v[24:25], v[24:25], 0, s[18:19]
	s_nop 0
	v_lshlrev_b32_e32 v28, 16, v30
	v_and_b32_e32 v29, 0xffff0000, v30
	s_nop 0
	v_lshlrev_b32_e32 v54, 16, v42
	v_and_b32_e32 v55, 0xffff0000, v42
	v_and_b32_e32 v30, 0xffff0000, v31
	v_lshlrev_b32_e32 v31, 16, v31
	v_and_b32_e32 v42, 0xffff0000, v43
	v_lshlrev_b32_e32 v43, 16, v43
	v_pk_mul_f32 v[60:61], v[28:29], v[28:29]
	v_pk_mul_f32 v[64:65], v[54:55], v[54:55]
	s_nop 0
	v_lshlrev_b32_e32 v19, 16, v40
	v_and_b32_e32 v39, 0xffff0000, v40
	v_lshlrev_b32_e32 v40, 16, v41
	v_and_b32_e32 v41, 0xffff0000, v41
	v_lshlrev_b32_e32 v56, 16, v44
	v_and_b32_e32 v57, 0xffff0000, v44
	v_lshlrev_b32_e32 v58, 16, v46
	v_and_b32_e32 v59, 0xffff0000, v46
	v_pk_mul_f32 v[62:63], v[30:31], v[30:31]
	v_pk_mul_f32 v[66:67], v[42:43], v[42:43]
	v_mul_f32_e32 v86, 0xbfb8aa3b, v40
	v_mul_f32_e32 v87, 0xbfb8aa3b, v41
	v_mov_b32_e32 v40, v64
	v_mov_b32_e32 v41, v60
	v_mov_b32_e32 v60, v65
	v_and_b32_e32 v44, 0xffff0000, v45
	v_lshlrev_b32_e32 v45, 16, v45
	v_and_b32_e32 v46, 0xffff0000, v47
	v_lshlrev_b32_e32 v47, 16, v47
	v_pk_mul_f32 v[68:69], v[56:57], v[56:57]
	v_pk_mul_f32 v[72:73], v[58:59], v[58:59]
	s_nop 0
	v_lshlrev_b32_e32 v76, 16, v48
	v_and_b32_e32 v77, 0xffff0000, v48
	v_lshlrev_b32_e32 v78, 16, v49
	v_and_b32_e32 v79, 0xffff0000, v49
	s_nop 0
	v_lshlrev_b32_e32 v80, 16, v50
	v_and_b32_e32 v50, 0xffff0000, v50
	v_lshlrev_b32_e32 v81, 16, v51
	v_and_b32_e32 v51, 0xffff0000, v51
	v_mov_b32_e32 v48, v67
	v_mov_b32_e32 v49, v63
	v_pk_add_f32 v[40:41], v[40:41], v[60:61]
	v_pk_mul_f32 v[70:71], v[44:45], v[44:45]
	v_pk_mul_f32 v[74:75], v[46:47], v[46:47]
	v_mov_b32_e32 v67, v62
	v_mul_f32_e32 v63, 0xbfb8aa3b, v77
	v_mul_f32_e32 v65, 0xbfb8aa3b, v79
	v_mul_f32_e32 v77, 0xbfb8aa3b, v50
	v_mul_f32_e32 v79, 0xbfb8aa3b, v51
	v_mov_b32_e32 v50, v72
	v_mov_b32_e32 v51, v68
	v_mov_b32_e32 v68, v73
	v_pk_add_f32 v[40:41], v[48:49], v[40:41]
	s_nop 0
	v_lshlrev_b32_e32 v82, 16, v52
	v_and_b32_e32 v83, 0xffff0000, v52
	v_lshlrev_b32_e32 v84, 16, v53
	v_and_b32_e32 v85, 0xffff0000, v53
	v_mov_b32_e32 v52, v75
	v_mov_b32_e32 v53, v71
	v_pk_add_f32 v[50:51], v[50:51], v[68:69]
	v_pk_add_f32 v[40:41], v[66:67], v[40:41]
	v_pk_add_f32 v[48:49], v[52:53], v[50:51]
	ds_bpermute_b32 v51, v1, v41
	ds_bpermute_b32 v50, v1, v40
	v_mov_b32_e32 v75, v70
	v_pk_add_f32 v[48:49], v[74:75], v[48:49]
	ds_bpermute_b32 v53, v1, v49
	ds_bpermute_b32 v52, v1, v48
	s_waitcnt lgkmcnt(2)
	v_pk_add_f32 v[40:41], v[40:41], v[50:51]
	ds_bpermute_b32 v51, v34, v41
	ds_bpermute_b32 v50, v34, v40
	v_mul_f32_e32 v19, 0xbfb8aa3b, v19
	s_waitcnt lgkmcnt(2)
	v_pk_add_f32 v[48:49], v[48:49], v[52:53]
	ds_bpermute_b32 v53, v34, v49
	ds_bpermute_b32 v52, v34, v48
	s_waitcnt lgkmcnt(2)
	v_pk_add_f32 v[40:41], v[40:41], v[50:51]
	ds_bpermute_b32 v51, v35, v41
	ds_bpermute_b32 v50, v35, v40
	v_mul_f32_e32 v39, 0xbfb8aa3b, v39
	s_waitcnt lgkmcnt(2)
	v_pk_add_f32 v[48:49], v[48:49], v[52:53]
	ds_bpermute_b32 v53, v35, v49
	ds_bpermute_b32 v52, v35, v48
	s_waitcnt lgkmcnt(2)
	v_pk_add_f32 v[40:41], v[40:41], v[50:51]
	ds_bpermute_b32 v51, v36, v41
	ds_bpermute_b32 v50, v36, v40
	v_mul_f32_e32 v62, 0xbfb8aa3b, v76
	s_waitcnt lgkmcnt(2)
	v_pk_add_f32 v[48:49], v[48:49], v[52:53]
	ds_bpermute_b32 v53, v36, v49
	ds_bpermute_b32 v52, v36, v48
	s_waitcnt lgkmcnt(2)
	v_pk_add_f32 v[40:41], v[40:41], v[50:51]
	ds_bpermute_b32 v51, v37, v41
	ds_bpermute_b32 v50, v37, v40
	v_mul_f32_e32 v76, 0xbfb8aa3b, v80
	s_waitcnt lgkmcnt(2)
	v_pk_add_f32 v[48:49], v[48:49], v[52:53]
	ds_bpermute_b32 v53, v37, v49
	ds_bpermute_b32 v52, v37, v48
	s_waitcnt lgkmcnt(2)
	v_pk_add_f32 v[40:41], v[40:41], v[50:51]
	ds_bpermute_b32 v51, v38, v41
	ds_bpermute_b32 v50, v38, v40
	v_exp_f32_e32 v19, v19
	s_waitcnt lgkmcnt(2)
	v_pk_add_f32 v[48:49], v[48:49], v[52:53]
	ds_bpermute_b32 v53, v38, v49
	ds_bpermute_b32 v52, v38, v48
	s_waitcnt lgkmcnt(2)
	v_pk_add_f32 v[40:41], v[40:41], v[50:51]
	v_exp_f32_e32 v39, v39
	v_pk_fma_f32 v[40:41], v[40:41], s[22:23], v[26:27] op_sel_hi:[1,0,0]
	v_exp_f32_e32 v80, v86
	v_mul_f32_e32 v50, 0x4b800000, v41
	v_cmp_gt_f32_e64 s[8:9], s15, v41
	s_waitcnt lgkmcnt(0)
	v_pk_add_f32 v[48:49], v[48:49], v[52:53]
	v_mul_f32_e32 v64, 0xbfb8aa3b, v78
	v_cndmask_b32_e64 v41, v41, v50, s[8:9]
	v_mul_f32_e32 v78, 0xbfb8aa3b, v81
	v_exp_f32_e32 v81, v87
	v_pk_fma_f32 v[48:49], v[48:49], s[22:23], v[26:27] op_sel_hi:[1,0,0]
	v_mul_f32_e32 v51, 0x4b800000, v40
	v_cmp_gt_f32_e32 vcc, s15, v40
	v_rsq_f32_e32 v41, v41
	v_exp_f32_e32 v60, v62
	v_exp_f32_e32 v61, v63
	v_exp_f32_e32 v62, v64
	v_exp_f32_e32 v63, v65
	v_mul_f32_e32 v52, 0x4b800000, v49
	v_mul_f32_e32 v53, 0x4b800000, v48
	v_cmp_gt_f32_e64 s[4:5], s15, v48
	v_cmp_gt_f32_e64 s[6:7], s15, v49
	v_cndmask_b32_e32 v40, v40, v51, vcc
	v_mul_f32_e32 v70, 0xbfb8aa3b, v82
	v_mul_f32_e32 v71, 0xbfb8aa3b, v83
	v_mul_f32_e32 v72, 0xbfb8aa3b, v84
	v_mul_f32_e32 v73, 0xbfb8aa3b, v85
	v_exp_f32_e32 v64, v76
	v_exp_f32_e32 v65, v77
	v_exp_f32_e32 v76, v78
	v_exp_f32_e32 v77, v79
	v_cndmask_b32_e64 v49, v49, v52, s[6:7]
	v_cndmask_b32_e64 v48, v48, v53, s[4:5]
	v_rsq_f32_e32 v40, v40
	v_exp_f32_e32 v68, v70
	v_exp_f32_e32 v69, v71
	v_exp_f32_e32 v70, v72
	v_exp_f32_e32 v71, v73
	v_add_f32_e32 v19, 1.0, v19
	v_add_f32_e32 v39, 1.0, v39
	v_add_f32_e32 v66, 1.0, v80
	v_rsq_f32_e32 v49, v49
	v_rsq_f32_e32 v48, v48
	v_add_f32_e32 v67, 1.0, v81
	v_rcp_f32_e32 v19, v19
	v_rcp_f32_e32 v39, v39
	v_rcp_f32_e32 v66, v66
	v_mul_f32_e32 v50, 0x45800000, v41
	v_add_f32_e32 v60, 1.0, v60
	v_add_f32_e32 v61, 1.0, v61
	v_add_f32_e32 v62, 1.0, v62
	v_add_f32_e32 v63, 1.0, v63
	v_rcp_f32_e32 v67, v67
	v_cndmask_b32_e64 v41, v41, v50, s[8:9]
	v_add_f32_e32 v64, 1.0, v64
	v_add_f32_e32 v65, 1.0, v65
	v_add_f32_e32 v72, 1.0, v76
	v_add_f32_e32 v73, 1.0, v77
	v_rcp_f32_e32 v60, v60
	v_rcp_f32_e32 v61, v61
	v_rcp_f32_e32 v62, v62
	v_rcp_f32_e32 v63, v63
	v_mul_f32_e32 v51, 0x45800000, v40
	v_mul_f32_e32 v28, v41, v28
	v_mul_f32_e32 v29, v41, v29
	v_mul_f32_e32 v31, v41, v31
	v_add_f32_e32 v68, 1.0, v68
	v_add_f32_e32 v69, 1.0, v69
	v_add_f32_e32 v70, 1.0, v70
	v_add_f32_e32 v71, 1.0, v71
	v_rcp_f32_e32 v64, v64
	v_rcp_f32_e32 v65, v65
	v_rcp_f32_e32 v72, v72
	v_rcp_f32_e32 v73, v73
	v_mul_f32_e32 v52, 0x45800000, v49
	v_mul_f32_e32 v53, 0x45800000, v48
	v_cndmask_b32_e32 v40, v40, v51, vcc
	v_mul_f32_e32 v30, v41, v30
	v_mul_f32_e32 v28, v14, v28
	v_mul_f32_e32 v29, v15, v29
	v_mul_f32_e32 v31, v16, v31
	v_rcp_f32_e32 v68, v68
	v_rcp_f32_e32 v69, v69
	v_rcp_f32_e32 v70, v70
	v_rcp_f32_e32 v71, v71
	v_cndmask_b32_e64 v49, v49, v52, s[6:7]
	v_cndmask_b32_e64 v48, v48, v53, s[4:5]
	v_mul_f32_e32 v41, v40, v54
	v_mul_f32_e32 v50, v40, v55
	v_mul_f32_e32 v43, v40, v43
	v_mul_f32_e32 v40, v40, v42
	v_mul_f32_e32 v30, v17, v30
	v_mul_f32_e32 v19, v19, v28
	v_mul_f32_e32 v28, v39, v29
	v_mul_f32_e32 v29, v66, v31
	v_mul_f32_e32 v42, v49, v56
	v_mul_f32_e32 v51, v49, v57
	v_mul_f32_e32 v45, v49, v45
	v_mul_f32_e32 v44, v49, v44
	v_mul_f32_e32 v49, v48, v58
	v_mul_f32_e32 v52, v48, v59
	v_mul_f32_e32 v47, v48, v47
	v_mul_f32_e32 v46, v48, v46
	v_mul_f32_e32 v41, v10, v41
	v_mul_f32_e32 v48, v11, v50
	v_mul_f32_e32 v43, v12, v43
	v_mul_f32_e32 v40, v13, v40
	v_mul_f32_e32 v30, v67, v30
	v_cvt_pk_bf16_f32 v28, v19, v28
	v_cvt_pk_bf16_f32 v29, v29, v30
	v_mul_f32_e32 v42, v6, v42
	v_mul_f32_e32 v50, v7, v51
	v_mul_f32_e32 v45, v8, v45
	v_mul_f32_e32 v44, v9, v44
	v_mul_f32_e32 v31, v60, v41
	v_mul_f32_e32 v39, v61, v48
	v_mul_f32_e32 v41, v62, v43
	v_mul_f32_e32 v40, v63, v40
	global_store_dwordx2 v[32:33], v[28:29], off
	v_cvt_pk_bf16_f32 v28, v31, v39
	v_cvt_pk_bf16_f32 v29, v41, v40
	v_mul_f32_e32 v49, v2, v49
	v_mul_f32_e32 v51, v3, v52
	v_mul_f32_e32 v47, v4, v47
	v_mul_f32_e32 v46, v5, v46
	v_mul_f32_e32 v42, v64, v42
	v_mul_f32_e32 v43, v65, v50
	v_mul_f32_e32 v45, v72, v45
	v_mul_f32_e32 v44, v73, v44
	global_store_dwordx2 v[32:33], v[28:29], off offset:512
	v_cvt_pk_bf16_f32 v28, v42, v43
	v_cvt_pk_bf16_f32 v29, v45, v44
	v_mul_f32_e32 v48, v68, v49
	v_mul_f32_e32 v49, v69, v51
	v_mul_f32_e32 v47, v70, v47
	v_mul_f32_e32 v46, v71, v46
	global_store_dwordx2 v[32:33], v[28:29], off offset:1024
	v_cvt_pk_bf16_f32 v28, v48, v49
	v_cvt_pk_bf16_f32 v29, v47, v46
	global_store_dwordx2 v[32:33], v[28:29], off offset:1536
	s_andn2_b64 exec, exec, s[20:21]
	s_nop 0
	v_lshl_add_u64 v[30:31], v[24:25], 0, v[20:21]
	v_add_co_u32_e32 v40, vcc, 0x3ec4a000, v30
	v_lshl_add_u64 v[28:29], v[22:23], 0, v[20:21]
	v_add_co_u32_e64 v32, s[4:5], s23, v30
	v_addc_co_u32_e32 v41, vcc, 0, v31, vcc
	s_nop 0
	v_addc_co_u32_e64 v33, s[4:5], 0, v31, s[4:5]
	v_add_co_u32_e32 v28, vcc, 0x42c4b000, v28
	s_waitcnt vmcnt(16)
	v_mov_b32_e32 v30, v128
	v_mov_b32_e32 v31, v129
	v_mov_b32_e32 v42, v130
	v_mov_b32_e32 v43, v131
	v_mov_b32_e32 v44, v132
	v_mov_b32_e32 v45, v133
	v_mov_b32_e32 v46, v134
	v_mov_b32_e32 v47, v135
	v_mov_b32_e32 v40, v136
	v_mov_b32_e32 v41, v137
	v_mov_b32_e32 v48, v138
	v_mov_b32_e32 v49, v139
	v_mov_b32_e32 v50, v140
	v_mov_b32_e32 v51, v141
	v_mov_b32_e32 v52, v142
	v_mov_b32_e32 v53, v143
	v_addc_co_u32_e32 v29, vcc, 0, v29, vcc
	v_add_u32_e32 v18, s14, v18
	v_cmp_lt_i32_e64 s[4:5], s24, v18
	s_or_b64 s[20:21], s[4:5], s[20:21]
	v_lshl_add_u64 v[22:23], v[22:23], 0, s[16:17]
	v_lshl_add_u64 v[24:25], v[24:25], 0, s[18:19]
	s_nop 0
	v_lshlrev_b32_e32 v28, 16, v30
	v_and_b32_e32 v29, 0xffff0000, v30
	s_nop 0
	v_lshlrev_b32_e32 v54, 16, v42
	v_and_b32_e32 v55, 0xffff0000, v42
	v_and_b32_e32 v30, 0xffff0000, v31
	v_lshlrev_b32_e32 v31, 16, v31
	v_and_b32_e32 v42, 0xffff0000, v43
	v_lshlrev_b32_e32 v43, 16, v43
	v_pk_mul_f32 v[60:61], v[28:29], v[28:29]
	v_pk_mul_f32 v[64:65], v[54:55], v[54:55]
	s_nop 0
	v_lshlrev_b32_e32 v19, 16, v40
	v_and_b32_e32 v39, 0xffff0000, v40
	v_lshlrev_b32_e32 v40, 16, v41
	v_and_b32_e32 v41, 0xffff0000, v41
	v_lshlrev_b32_e32 v56, 16, v44
	v_and_b32_e32 v57, 0xffff0000, v44
	v_lshlrev_b32_e32 v58, 16, v46
	v_and_b32_e32 v59, 0xffff0000, v46
	v_pk_mul_f32 v[62:63], v[30:31], v[30:31]
	v_pk_mul_f32 v[66:67], v[42:43], v[42:43]
	v_mul_f32_e32 v86, 0xbfb8aa3b, v40
	v_mul_f32_e32 v87, 0xbfb8aa3b, v41
	v_mov_b32_e32 v40, v64
	v_mov_b32_e32 v41, v60
	v_mov_b32_e32 v60, v65
	v_and_b32_e32 v44, 0xffff0000, v45
	v_lshlrev_b32_e32 v45, 16, v45
	v_and_b32_e32 v46, 0xffff0000, v47
	v_lshlrev_b32_e32 v47, 16, v47
	v_pk_mul_f32 v[68:69], v[56:57], v[56:57]
	v_pk_mul_f32 v[72:73], v[58:59], v[58:59]
	s_nop 0
	v_lshlrev_b32_e32 v76, 16, v48
	v_and_b32_e32 v77, 0xffff0000, v48
	v_lshlrev_b32_e32 v78, 16, v49
	v_and_b32_e32 v79, 0xffff0000, v49
	s_nop 0
	v_lshlrev_b32_e32 v80, 16, v50
	v_and_b32_e32 v50, 0xffff0000, v50
	v_lshlrev_b32_e32 v81, 16, v51
	v_and_b32_e32 v51, 0xffff0000, v51
	v_mov_b32_e32 v48, v67
	v_mov_b32_e32 v49, v63
	v_pk_add_f32 v[40:41], v[40:41], v[60:61]
	v_pk_mul_f32 v[70:71], v[44:45], v[44:45]
	v_pk_mul_f32 v[74:75], v[46:47], v[46:47]
	v_mov_b32_e32 v67, v62
	v_mul_f32_e32 v63, 0xbfb8aa3b, v77
	v_mul_f32_e32 v65, 0xbfb8aa3b, v79
	v_mul_f32_e32 v77, 0xbfb8aa3b, v50
	v_mul_f32_e32 v79, 0xbfb8aa3b, v51
	v_mov_b32_e32 v50, v72
	v_mov_b32_e32 v51, v68
	v_mov_b32_e32 v68, v73
	v_pk_add_f32 v[40:41], v[48:49], v[40:41]
	s_nop 0
	v_lshlrev_b32_e32 v82, 16, v52
	v_and_b32_e32 v83, 0xffff0000, v52
	v_lshlrev_b32_e32 v84, 16, v53
	v_and_b32_e32 v85, 0xffff0000, v53
	v_mov_b32_e32 v52, v75
	v_mov_b32_e32 v53, v71
	v_pk_add_f32 v[50:51], v[50:51], v[68:69]
	v_pk_add_f32 v[40:41], v[66:67], v[40:41]
	v_pk_add_f32 v[48:49], v[52:53], v[50:51]
	ds_bpermute_b32 v51, v1, v41
	ds_bpermute_b32 v50, v1, v40
	v_mov_b32_e32 v75, v70
	v_pk_add_f32 v[48:49], v[74:75], v[48:49]
	ds_bpermute_b32 v53, v1, v49
	ds_bpermute_b32 v52, v1, v48
	s_waitcnt lgkmcnt(2)
	v_pk_add_f32 v[40:41], v[40:41], v[50:51]
	ds_bpermute_b32 v51, v34, v41
	ds_bpermute_b32 v50, v34, v40
	v_mul_f32_e32 v19, 0xbfb8aa3b, v19
	s_waitcnt lgkmcnt(2)
	v_pk_add_f32 v[48:49], v[48:49], v[52:53]
	ds_bpermute_b32 v53, v34, v49
	ds_bpermute_b32 v52, v34, v48
	s_waitcnt lgkmcnt(2)
	v_pk_add_f32 v[40:41], v[40:41], v[50:51]
	ds_bpermute_b32 v51, v35, v41
	ds_bpermute_b32 v50, v35, v40
	v_mul_f32_e32 v39, 0xbfb8aa3b, v39
	s_waitcnt lgkmcnt(2)
	v_pk_add_f32 v[48:49], v[48:49], v[52:53]
	ds_bpermute_b32 v53, v35, v49
	ds_bpermute_b32 v52, v35, v48
	s_waitcnt lgkmcnt(2)
	v_pk_add_f32 v[40:41], v[40:41], v[50:51]
	ds_bpermute_b32 v51, v36, v41
	ds_bpermute_b32 v50, v36, v40
	v_mul_f32_e32 v62, 0xbfb8aa3b, v76
	s_waitcnt lgkmcnt(2)
	v_pk_add_f32 v[48:49], v[48:49], v[52:53]
	ds_bpermute_b32 v53, v36, v49
	ds_bpermute_b32 v52, v36, v48
	s_waitcnt lgkmcnt(2)
	v_pk_add_f32 v[40:41], v[40:41], v[50:51]
	ds_bpermute_b32 v51, v37, v41
	ds_bpermute_b32 v50, v37, v40
	v_mul_f32_e32 v76, 0xbfb8aa3b, v80
	s_waitcnt lgkmcnt(2)
	v_pk_add_f32 v[48:49], v[48:49], v[52:53]
	ds_bpermute_b32 v53, v37, v49
	ds_bpermute_b32 v52, v37, v48
	s_waitcnt lgkmcnt(2)
	v_pk_add_f32 v[40:41], v[40:41], v[50:51]
	ds_bpermute_b32 v51, v38, v41
	ds_bpermute_b32 v50, v38, v40
	v_exp_f32_e32 v19, v19
	s_waitcnt lgkmcnt(2)
	v_pk_add_f32 v[48:49], v[48:49], v[52:53]
	ds_bpermute_b32 v53, v38, v49
	ds_bpermute_b32 v52, v38, v48
	s_waitcnt lgkmcnt(2)
	v_pk_add_f32 v[40:41], v[40:41], v[50:51]
	v_exp_f32_e32 v39, v39
	v_pk_fma_f32 v[40:41], v[40:41], s[22:23], v[26:27] op_sel_hi:[1,0,0]
	v_exp_f32_e32 v80, v86
	v_mul_f32_e32 v50, 0x4b800000, v41
	v_cmp_gt_f32_e64 s[8:9], s15, v41
	s_waitcnt lgkmcnt(0)
	v_pk_add_f32 v[48:49], v[48:49], v[52:53]
	v_mul_f32_e32 v64, 0xbfb8aa3b, v78
	v_cndmask_b32_e64 v41, v41, v50, s[8:9]
	v_mul_f32_e32 v78, 0xbfb8aa3b, v81
	v_exp_f32_e32 v81, v87
	v_pk_fma_f32 v[48:49], v[48:49], s[22:23], v[26:27] op_sel_hi:[1,0,0]
	v_mul_f32_e32 v51, 0x4b800000, v40
	v_cmp_gt_f32_e32 vcc, s15, v40
	v_rsq_f32_e32 v41, v41
	v_exp_f32_e32 v60, v62
	v_exp_f32_e32 v61, v63
	v_exp_f32_e32 v62, v64
	v_exp_f32_e32 v63, v65
	v_mul_f32_e32 v52, 0x4b800000, v49
	v_mul_f32_e32 v53, 0x4b800000, v48
	v_cmp_gt_f32_e64 s[4:5], s15, v48
	v_cmp_gt_f32_e64 s[6:7], s15, v49
	v_cndmask_b32_e32 v40, v40, v51, vcc
	v_mul_f32_e32 v70, 0xbfb8aa3b, v82
	v_mul_f32_e32 v71, 0xbfb8aa3b, v83
	v_mul_f32_e32 v72, 0xbfb8aa3b, v84
	v_mul_f32_e32 v73, 0xbfb8aa3b, v85
	v_exp_f32_e32 v64, v76
	v_exp_f32_e32 v65, v77
	v_exp_f32_e32 v76, v78
	v_exp_f32_e32 v77, v79
	v_cndmask_b32_e64 v49, v49, v52, s[6:7]
	v_cndmask_b32_e64 v48, v48, v53, s[4:5]
	v_rsq_f32_e32 v40, v40
	v_exp_f32_e32 v68, v70
	v_exp_f32_e32 v69, v71
	v_exp_f32_e32 v70, v72
	v_exp_f32_e32 v71, v73
	v_add_f32_e32 v19, 1.0, v19
	v_add_f32_e32 v39, 1.0, v39
	v_add_f32_e32 v66, 1.0, v80
	v_rsq_f32_e32 v49, v49
	v_rsq_f32_e32 v48, v48
	v_add_f32_e32 v67, 1.0, v81
	v_rcp_f32_e32 v19, v19
	v_rcp_f32_e32 v39, v39
	v_rcp_f32_e32 v66, v66
	v_mul_f32_e32 v50, 0x45800000, v41
	v_add_f32_e32 v60, 1.0, v60
	v_add_f32_e32 v61, 1.0, v61
	v_add_f32_e32 v62, 1.0, v62
	v_add_f32_e32 v63, 1.0, v63
	v_rcp_f32_e32 v67, v67
	v_cndmask_b32_e64 v41, v41, v50, s[8:9]
	v_add_f32_e32 v64, 1.0, v64
	v_add_f32_e32 v65, 1.0, v65
	v_add_f32_e32 v72, 1.0, v76
	v_add_f32_e32 v73, 1.0, v77
	v_rcp_f32_e32 v60, v60
	v_rcp_f32_e32 v61, v61
	v_rcp_f32_e32 v62, v62
	v_rcp_f32_e32 v63, v63
	v_mul_f32_e32 v51, 0x45800000, v40
	v_mul_f32_e32 v28, v41, v28
	v_mul_f32_e32 v29, v41, v29
	v_mul_f32_e32 v31, v41, v31
	v_add_f32_e32 v68, 1.0, v68
	v_add_f32_e32 v69, 1.0, v69
	v_add_f32_e32 v70, 1.0, v70
	v_add_f32_e32 v71, 1.0, v71
	v_rcp_f32_e32 v64, v64
	v_rcp_f32_e32 v65, v65
	v_rcp_f32_e32 v72, v72
	v_rcp_f32_e32 v73, v73
	v_mul_f32_e32 v52, 0x45800000, v49
	v_mul_f32_e32 v53, 0x45800000, v48
	v_cndmask_b32_e32 v40, v40, v51, vcc
	v_mul_f32_e32 v30, v41, v30
	v_mul_f32_e32 v28, v14, v28
	v_mul_f32_e32 v29, v15, v29
	v_mul_f32_e32 v31, v16, v31
	v_rcp_f32_e32 v68, v68
	v_rcp_f32_e32 v69, v69
	v_rcp_f32_e32 v70, v70
	v_rcp_f32_e32 v71, v71
	v_cndmask_b32_e64 v49, v49, v52, s[6:7]
	v_cndmask_b32_e64 v48, v48, v53, s[4:5]
	v_mul_f32_e32 v41, v40, v54
	v_mul_f32_e32 v50, v40, v55
	v_mul_f32_e32 v43, v40, v43
	v_mul_f32_e32 v40, v40, v42
	v_mul_f32_e32 v30, v17, v30
	v_mul_f32_e32 v19, v19, v28
	v_mul_f32_e32 v28, v39, v29
	v_mul_f32_e32 v29, v66, v31
	v_mul_f32_e32 v42, v49, v56
	v_mul_f32_e32 v51, v49, v57
	v_mul_f32_e32 v45, v49, v45
	v_mul_f32_e32 v44, v49, v44
	v_mul_f32_e32 v49, v48, v58
	v_mul_f32_e32 v52, v48, v59
	v_mul_f32_e32 v47, v48, v47
	v_mul_f32_e32 v46, v48, v46
	v_mul_f32_e32 v41, v10, v41
	v_mul_f32_e32 v48, v11, v50
	v_mul_f32_e32 v43, v12, v43
	v_mul_f32_e32 v40, v13, v40
	v_mul_f32_e32 v30, v67, v30
	v_cvt_pk_bf16_f32 v28, v19, v28
	v_cvt_pk_bf16_f32 v29, v29, v30
	v_mul_f32_e32 v42, v6, v42
	v_mul_f32_e32 v50, v7, v51
	v_mul_f32_e32 v45, v8, v45
	v_mul_f32_e32 v44, v9, v44
	v_mul_f32_e32 v31, v60, v41
	v_mul_f32_e32 v39, v61, v48
	v_mul_f32_e32 v41, v62, v43
	v_mul_f32_e32 v40, v63, v40
	global_store_dwordx2 v[32:33], v[28:29], off
	v_cvt_pk_bf16_f32 v28, v31, v39
	v_cvt_pk_bf16_f32 v29, v41, v40
	v_mul_f32_e32 v49, v2, v49
	v_mul_f32_e32 v51, v3, v52
	v_mul_f32_e32 v47, v4, v47
	v_mul_f32_e32 v46, v5, v46
	v_mul_f32_e32 v42, v64, v42
	v_mul_f32_e32 v43, v65, v50
	v_mul_f32_e32 v45, v72, v45
	v_mul_f32_e32 v44, v73, v44
	global_store_dwordx2 v[32:33], v[28:29], off offset:512
	v_cvt_pk_bf16_f32 v28, v42, v43
	v_cvt_pk_bf16_f32 v29, v45, v44
	v_mul_f32_e32 v48, v68, v49
	v_mul_f32_e32 v49, v69, v51
	v_mul_f32_e32 v47, v70, v47
	v_mul_f32_e32 v46, v71, v46
	global_store_dwordx2 v[32:33], v[28:29], off offset:1024
	v_cvt_pk_bf16_f32 v28, v48, v49
	v_cvt_pk_bf16_f32 v29, v47, v46
	global_store_dwordx2 v[32:33], v[28:29], off offset:1536
	s_andn2_b64 exec, exec, s[20:21]
	s_nop 0
	v_lshl_add_u64 v[30:31], v[24:25], 0, v[20:21]
	v_add_co_u32_e32 v40, vcc, 0x3ec4a000, v30
	v_lshl_add_u64 v[28:29], v[22:23], 0, v[20:21]
	v_add_co_u32_e64 v32, s[4:5], s23, v30
	v_addc_co_u32_e32 v41, vcc, 0, v31, vcc
	s_nop 0
	v_addc_co_u32_e64 v33, s[4:5], 0, v31, s[4:5]
	v_add_co_u32_e32 v28, vcc, 0x42c4b000, v28
	s_waitcnt vmcnt(8)
	v_mov_b32_e32 v30, v144
	v_mov_b32_e32 v31, v145
	v_mov_b32_e32 v42, v146
	v_mov_b32_e32 v43, v147
	v_mov_b32_e32 v44, v148
	v_mov_b32_e32 v45, v149
	v_mov_b32_e32 v46, v150
	v_mov_b32_e32 v47, v151
	v_mov_b32_e32 v40, v152
	v_mov_b32_e32 v41, v153
	v_mov_b32_e32 v48, v154
	v_mov_b32_e32 v49, v155
	v_mov_b32_e32 v50, v156
	v_mov_b32_e32 v51, v157
	v_mov_b32_e32 v52, v158
	v_mov_b32_e32 v53, v159
	v_addc_co_u32_e32 v29, vcc, 0, v29, vcc
	v_add_u32_e32 v18, s14, v18
	v_cmp_lt_i32_e64 s[4:5], s24, v18
	s_or_b64 s[20:21], s[4:5], s[20:21]
	v_lshl_add_u64 v[22:23], v[22:23], 0, s[16:17]
	v_lshl_add_u64 v[24:25], v[24:25], 0, s[18:19]
	s_nop 0
	v_lshlrev_b32_e32 v28, 16, v30
	v_and_b32_e32 v29, 0xffff0000, v30
	s_nop 0
	v_lshlrev_b32_e32 v54, 16, v42
	v_and_b32_e32 v55, 0xffff0000, v42
	v_and_b32_e32 v30, 0xffff0000, v31
	v_lshlrev_b32_e32 v31, 16, v31
	v_and_b32_e32 v42, 0xffff0000, v43
	v_lshlrev_b32_e32 v43, 16, v43
	v_pk_mul_f32 v[60:61], v[28:29], v[28:29]
	v_pk_mul_f32 v[64:65], v[54:55], v[54:55]
	s_nop 0
	v_lshlrev_b32_e32 v19, 16, v40
	v_and_b32_e32 v39, 0xffff0000, v40
	v_lshlrev_b32_e32 v40, 16, v41
	v_and_b32_e32 v41, 0xffff0000, v41
	v_lshlrev_b32_e32 v56, 16, v44
	v_and_b32_e32 v57, 0xffff0000, v44
	v_lshlrev_b32_e32 v58, 16, v46
	v_and_b32_e32 v59, 0xffff0000, v46
	v_pk_mul_f32 v[62:63], v[30:31], v[30:31]
	v_pk_mul_f32 v[66:67], v[42:43], v[42:43]
	v_mul_f32_e32 v86, 0xbfb8aa3b, v40
	v_mul_f32_e32 v87, 0xbfb8aa3b, v41
	v_mov_b32_e32 v40, v64
	v_mov_b32_e32 v41, v60
	v_mov_b32_e32 v60, v65
	v_and_b32_e32 v44, 0xffff0000, v45
	v_lshlrev_b32_e32 v45, 16, v45
	v_and_b32_e32 v46, 0xffff0000, v47
	v_lshlrev_b32_e32 v47, 16, v47
	v_pk_mul_f32 v[68:69], v[56:57], v[56:57]
	v_pk_mul_f32 v[72:73], v[58:59], v[58:59]
	s_nop 0
	v_lshlrev_b32_e32 v76, 16, v48
	v_and_b32_e32 v77, 0xffff0000, v48
	v_lshlrev_b32_e32 v78, 16, v49
	v_and_b32_e32 v79, 0xffff0000, v49
	s_nop 0
	v_lshlrev_b32_e32 v80, 16, v50
	v_and_b32_e32 v50, 0xffff0000, v50
	v_lshlrev_b32_e32 v81, 16, v51
	v_and_b32_e32 v51, 0xffff0000, v51
	v_mov_b32_e32 v48, v67
	v_mov_b32_e32 v49, v63
	v_pk_add_f32 v[40:41], v[40:41], v[60:61]
	v_pk_mul_f32 v[70:71], v[44:45], v[44:45]
	v_pk_mul_f32 v[74:75], v[46:47], v[46:47]
	v_mov_b32_e32 v67, v62
	v_mul_f32_e32 v63, 0xbfb8aa3b, v77
	v_mul_f32_e32 v65, 0xbfb8aa3b, v79
	v_mul_f32_e32 v77, 0xbfb8aa3b, v50
	v_mul_f32_e32 v79, 0xbfb8aa3b, v51
	v_mov_b32_e32 v50, v72
	v_mov_b32_e32 v51, v68
	v_mov_b32_e32 v68, v73
	v_pk_add_f32 v[40:41], v[48:49], v[40:41]
	s_nop 0
	v_lshlrev_b32_e32 v82, 16, v52
	v_and_b32_e32 v83, 0xffff0000, v52
	v_lshlrev_b32_e32 v84, 16, v53
	v_and_b32_e32 v85, 0xffff0000, v53
	v_mov_b32_e32 v52, v75
	v_mov_b32_e32 v53, v71
	v_pk_add_f32 v[50:51], v[50:51], v[68:69]
	v_pk_add_f32 v[40:41], v[66:67], v[40:41]
	v_pk_add_f32 v[48:49], v[52:53], v[50:51]
	ds_bpermute_b32 v51, v1, v41
	ds_bpermute_b32 v50, v1, v40
	v_mov_b32_e32 v75, v70
	v_pk_add_f32 v[48:49], v[74:75], v[48:49]
	ds_bpermute_b32 v53, v1, v49
	ds_bpermute_b32 v52, v1, v48
	s_waitcnt lgkmcnt(2)
	v_pk_add_f32 v[40:41], v[40:41], v[50:51]
	ds_bpermute_b32 v51, v34, v41
	ds_bpermute_b32 v50, v34, v40
	v_mul_f32_e32 v19, 0xbfb8aa3b, v19
	s_waitcnt lgkmcnt(2)
	v_pk_add_f32 v[48:49], v[48:49], v[52:53]
	ds_bpermute_b32 v53, v34, v49
	ds_bpermute_b32 v52, v34, v48
	s_waitcnt lgkmcnt(2)
	v_pk_add_f32 v[40:41], v[40:41], v[50:51]
	ds_bpermute_b32 v51, v35, v41
	ds_bpermute_b32 v50, v35, v40
	v_mul_f32_e32 v39, 0xbfb8aa3b, v39
	s_waitcnt lgkmcnt(2)
	v_pk_add_f32 v[48:49], v[48:49], v[52:53]
	ds_bpermute_b32 v53, v35, v49
	ds_bpermute_b32 v52, v35, v48
	s_waitcnt lgkmcnt(2)
	v_pk_add_f32 v[40:41], v[40:41], v[50:51]
	ds_bpermute_b32 v51, v36, v41
	ds_bpermute_b32 v50, v36, v40
	v_mul_f32_e32 v62, 0xbfb8aa3b, v76
	s_waitcnt lgkmcnt(2)
	v_pk_add_f32 v[48:49], v[48:49], v[52:53]
	ds_bpermute_b32 v53, v36, v49
	ds_bpermute_b32 v52, v36, v48
	s_waitcnt lgkmcnt(2)
	v_pk_add_f32 v[40:41], v[40:41], v[50:51]
	ds_bpermute_b32 v51, v37, v41
	ds_bpermute_b32 v50, v37, v40
	v_mul_f32_e32 v76, 0xbfb8aa3b, v80
	s_waitcnt lgkmcnt(2)
	v_pk_add_f32 v[48:49], v[48:49], v[52:53]
	ds_bpermute_b32 v53, v37, v49
	ds_bpermute_b32 v52, v37, v48
	s_waitcnt lgkmcnt(2)
	v_pk_add_f32 v[40:41], v[40:41], v[50:51]
	ds_bpermute_b32 v51, v38, v41
	ds_bpermute_b32 v50, v38, v40
	v_exp_f32_e32 v19, v19
	s_waitcnt lgkmcnt(2)
	v_pk_add_f32 v[48:49], v[48:49], v[52:53]
	ds_bpermute_b32 v53, v38, v49
	ds_bpermute_b32 v52, v38, v48
	s_waitcnt lgkmcnt(2)
	v_pk_add_f32 v[40:41], v[40:41], v[50:51]
	v_exp_f32_e32 v39, v39
	v_pk_fma_f32 v[40:41], v[40:41], s[22:23], v[26:27] op_sel_hi:[1,0,0]
	v_exp_f32_e32 v80, v86
	v_mul_f32_e32 v50, 0x4b800000, v41
	v_cmp_gt_f32_e64 s[8:9], s15, v41
	s_waitcnt lgkmcnt(0)
	v_pk_add_f32 v[48:49], v[48:49], v[52:53]
	v_mul_f32_e32 v64, 0xbfb8aa3b, v78
	v_cndmask_b32_e64 v41, v41, v50, s[8:9]
	v_mul_f32_e32 v78, 0xbfb8aa3b, v81
	v_exp_f32_e32 v81, v87
	v_pk_fma_f32 v[48:49], v[48:49], s[22:23], v[26:27] op_sel_hi:[1,0,0]
	v_mul_f32_e32 v51, 0x4b800000, v40
	v_cmp_gt_f32_e32 vcc, s15, v40
	v_rsq_f32_e32 v41, v41
	v_exp_f32_e32 v60, v62
	v_exp_f32_e32 v61, v63
	v_exp_f32_e32 v62, v64
	v_exp_f32_e32 v63, v65
	v_mul_f32_e32 v52, 0x4b800000, v49
	v_mul_f32_e32 v53, 0x4b800000, v48
	v_cmp_gt_f32_e64 s[4:5], s15, v48
	v_cmp_gt_f32_e64 s[6:7], s15, v49
	v_cndmask_b32_e32 v40, v40, v51, vcc
	v_mul_f32_e32 v70, 0xbfb8aa3b, v82
	v_mul_f32_e32 v71, 0xbfb8aa3b, v83
	v_mul_f32_e32 v72, 0xbfb8aa3b, v84
	v_mul_f32_e32 v73, 0xbfb8aa3b, v85
	v_exp_f32_e32 v64, v76
	v_exp_f32_e32 v65, v77
	v_exp_f32_e32 v76, v78
	v_exp_f32_e32 v77, v79
	v_cndmask_b32_e64 v49, v49, v52, s[6:7]
	v_cndmask_b32_e64 v48, v48, v53, s[4:5]
	v_rsq_f32_e32 v40, v40
	v_exp_f32_e32 v68, v70
	v_exp_f32_e32 v69, v71
	v_exp_f32_e32 v70, v72
	v_exp_f32_e32 v71, v73
	v_add_f32_e32 v19, 1.0, v19
	v_add_f32_e32 v39, 1.0, v39
	v_add_f32_e32 v66, 1.0, v80
	v_rsq_f32_e32 v49, v49
	v_rsq_f32_e32 v48, v48
	v_add_f32_e32 v67, 1.0, v81
	v_rcp_f32_e32 v19, v19
	v_rcp_f32_e32 v39, v39
	v_rcp_f32_e32 v66, v66
	v_mul_f32_e32 v50, 0x45800000, v41
	v_add_f32_e32 v60, 1.0, v60
	v_add_f32_e32 v61, 1.0, v61
	v_add_f32_e32 v62, 1.0, v62
	v_add_f32_e32 v63, 1.0, v63
	v_rcp_f32_e32 v67, v67
	v_cndmask_b32_e64 v41, v41, v50, s[8:9]
	v_add_f32_e32 v64, 1.0, v64
	v_add_f32_e32 v65, 1.0, v65
	v_add_f32_e32 v72, 1.0, v76
	v_add_f32_e32 v73, 1.0, v77
	v_rcp_f32_e32 v60, v60
	v_rcp_f32_e32 v61, v61
	v_rcp_f32_e32 v62, v62
	v_rcp_f32_e32 v63, v63
	v_mul_f32_e32 v51, 0x45800000, v40
	v_mul_f32_e32 v28, v41, v28
	v_mul_f32_e32 v29, v41, v29
	v_mul_f32_e32 v31, v41, v31
	v_add_f32_e32 v68, 1.0, v68
	v_add_f32_e32 v69, 1.0, v69
	v_add_f32_e32 v70, 1.0, v70
	v_add_f32_e32 v71, 1.0, v71
	v_rcp_f32_e32 v64, v64
	v_rcp_f32_e32 v65, v65
	v_rcp_f32_e32 v72, v72
	v_rcp_f32_e32 v73, v73
	v_mul_f32_e32 v52, 0x45800000, v49
	v_mul_f32_e32 v53, 0x45800000, v48
	v_cndmask_b32_e32 v40, v40, v51, vcc
	v_mul_f32_e32 v30, v41, v30
	v_mul_f32_e32 v28, v14, v28
	v_mul_f32_e32 v29, v15, v29
	v_mul_f32_e32 v31, v16, v31
	v_rcp_f32_e32 v68, v68
	v_rcp_f32_e32 v69, v69
	v_rcp_f32_e32 v70, v70
	v_rcp_f32_e32 v71, v71
	v_cndmask_b32_e64 v49, v49, v52, s[6:7]
	v_cndmask_b32_e64 v48, v48, v53, s[4:5]
	v_mul_f32_e32 v41, v40, v54
	v_mul_f32_e32 v50, v40, v55
	v_mul_f32_e32 v43, v40, v43
	v_mul_f32_e32 v40, v40, v42
	v_mul_f32_e32 v30, v17, v30
	v_mul_f32_e32 v19, v19, v28
	v_mul_f32_e32 v28, v39, v29
	v_mul_f32_e32 v29, v66, v31
	v_mul_f32_e32 v42, v49, v56
	v_mul_f32_e32 v51, v49, v57
	v_mul_f32_e32 v45, v49, v45
	v_mul_f32_e32 v44, v49, v44
	v_mul_f32_e32 v49, v48, v58
	v_mul_f32_e32 v52, v48, v59
	v_mul_f32_e32 v47, v48, v47
	v_mul_f32_e32 v46, v48, v46
	v_mul_f32_e32 v41, v10, v41
	v_mul_f32_e32 v48, v11, v50
	v_mul_f32_e32 v43, v12, v43
	v_mul_f32_e32 v40, v13, v40
	v_mul_f32_e32 v30, v67, v30
	v_cvt_pk_bf16_f32 v28, v19, v28
	v_cvt_pk_bf16_f32 v29, v29, v30
	v_mul_f32_e32 v42, v6, v42
	v_mul_f32_e32 v50, v7, v51
	v_mul_f32_e32 v45, v8, v45
	v_mul_f32_e32 v44, v9, v44
	v_mul_f32_e32 v31, v60, v41
	v_mul_f32_e32 v39, v61, v48
	v_mul_f32_e32 v41, v62, v43
	v_mul_f32_e32 v40, v63, v40
	global_store_dwordx2 v[32:33], v[28:29], off
	v_cvt_pk_bf16_f32 v28, v31, v39
	v_cvt_pk_bf16_f32 v29, v41, v40
	v_mul_f32_e32 v49, v2, v49
	v_mul_f32_e32 v51, v3, v52
	v_mul_f32_e32 v47, v4, v47
	v_mul_f32_e32 v46, v5, v46
	v_mul_f32_e32 v42, v64, v42
	v_mul_f32_e32 v43, v65, v50
	v_mul_f32_e32 v45, v72, v45
	v_mul_f32_e32 v44, v73, v44
	global_store_dwordx2 v[32:33], v[28:29], off offset:512
	v_cvt_pk_bf16_f32 v28, v42, v43
	v_cvt_pk_bf16_f32 v29, v45, v44
	v_mul_f32_e32 v48, v68, v49
	v_mul_f32_e32 v49, v69, v51
	v_mul_f32_e32 v47, v70, v47
	v_mul_f32_e32 v46, v71, v46
	global_store_dwordx2 v[32:33], v[28:29], off offset:1024
	v_cvt_pk_bf16_f32 v28, v48, v49
	v_cvt_pk_bf16_f32 v29, v47, v46
	global_store_dwordx2 v[32:33], v[28:29], off offset:1536
	s_andn2_b64 exec, exec, s[20:21]
